# adds: barrier census block moved out of line, leader release tail duplicated (no cold branch), GELU row statistics with packed adds and fused squares
# speedup vs baseline: 1.0364x; 1.0036x over previous
.LBB0_90:
	s_cmp_lt_i32 s28, 2
	s_cselect_b64 s[0:1], -1, 0
	s_cmp_gt_i32 s29, 2
	s_cselect_b64 s[4:5], -1, 0
	s_and_b64 s[0:1], s[0:1], s[4:5]
	s_andn2_b64 vcc, exec, s[0:1]
	s_cbranch_vccnz .LBB0_240
	s_waitcnt vmcnt(0)
	s_barrier
	s_getreg_b32 s0, hwreg(HW_REG_HW_ID, 0, 6)
	s_lshl_b32 s0, s0, 2
	s_and_b32 s0, s0, 0xfc
	s_add_i32 s0, s0, 0
	s_add_i32 s0, s0, 0x25c00
	v_mov_b32_e32 v0, s0
	ds_read_b32 v0, v0
	s_waitcnt lgkmcnt(0)
	v_readfirstlane_b32 s0, v0
	v_mbcnt_lo_u32_b32 v0, -1, 0
	v_mbcnt_hi_u32_b32 v0, -1, v0
	s_nop 1
	v_lshl_add_u32 v0, s0, 6, v0
	s_nop 0
	v_cmp_eq_u32_e32 vcc, 0, v0
	s_and_saveexec_b64 s[6:7], vcc
	s_cbranch_execz .LBB0_119
	s_add_i32 s0, 0, 0x24800
	v_mov_b32_e32 v0, s0
	s_waitcnt vmcnt(0) expcnt(0) lgkmcnt(0)
	ds_read_b32 v1, v0
	s_add_i32 s0, 0, 0x24804
	v_mov_b32_e32 v0, s0
	ds_read_b32 v0, v0
	s_waitcnt lgkmcnt(1)
	v_cmp_ne_u32_e32 vcc, 0, v1
	s_cbranch_vccz .Lcensus_0

.Lcensus_0:
	v_readlane_b32 s0, v249, 0
	v_readlane_b32 s1, v249, 1
	s_load_dwordx2 s[10:11], s[0:1], 0x4
	s_add_u32 s0, s94, 0x1000
	s_addc_u32 s1, s95, 0
	s_add_u32 s8, s94, 0x1100
	s_addc_u32 s9, s95, 0
	s_waitcnt lgkmcnt(0)
	s_mul_i32 s3, s10, s33
	s_add_u32 s10, s94, 0x1200
	s_mul_i32 s3, s3, s11
	s_addc_u32 s11, s95, 0
	s_add_u32 s12, s94, 0x1300
	s_addc_u32 s13, s95, 0
	s_mov_b32 s20, 1
	v_mov_b32_e32 v16, 0
	s_branch .LBB0_95

.LBB0_106:
	v_readlane_b32 s0, v249, 34
	s_cmp_eq_u32 s0, 0
	s_cselect_b64 vcc, -1, 0
	s_cmp_eq_u32 s0, 1
	v_cndmask_b32_e32 v16, 0, v15, vcc
	s_cselect_b64 vcc, -1, 0
	s_cmp_eq_u32 s0, 2
	v_cndmask_b32_e32 v16, v16, v0, vcc
	s_cselect_b64 vcc, -1, 0
	s_cmp_eq_u32 s0, 3
	v_cndmask_b32_e32 v16, v16, v1, vcc
	s_cselect_b64 vcc, -1, 0
	s_cmp_eq_u32 s0, 4
	v_cndmask_b32_e32 v16, v16, v2, vcc
	s_cselect_b64 vcc, -1, 0
	s_cmp_eq_u32 s0, 5
	v_cndmask_b32_e32 v16, v16, v3, vcc
	s_cselect_b64 vcc, -1, 0
	s_cmp_eq_u32 s0, 6
	v_cndmask_b32_e32 v16, v16, v4, vcc
	s_cselect_b64 vcc, -1, 0
	s_cmp_eq_u32 s0, 7
	v_cndmask_b32_e32 v16, v16, v5, vcc
	s_cselect_b64 vcc, -1, 0
	s_cmp_eq_u32 s0, 8
	v_cndmask_b32_e32 v16, v16, v6, vcc
	s_cselect_b64 vcc, -1, 0
	s_cmp_eq_u32 s0, 9
	v_cndmask_b32_e32 v16, v16, v7, vcc
	s_cselect_b64 vcc, -1, 0
	s_cmp_eq_u32 s0, 10
	v_cndmask_b32_e32 v16, v16, v8, vcc
	s_cselect_b64 vcc, -1, 0
	s_cmp_eq_u32 s0, 11
	v_cndmask_b32_e32 v16, v16, v9, vcc
	s_cselect_b64 vcc, -1, 0
	s_cmp_eq_u32 s0, 12
	v_cndmask_b32_e32 v16, v16, v10, vcc
	s_cselect_b64 vcc, -1, 0
	s_cmp_eq_u32 s0, 13
	v_cndmask_b32_e32 v16, v16, v11, vcc
	s_cselect_b64 vcc, -1, 0
	s_cmp_eq_u32 s0, 14
	v_cndmask_b32_e32 v16, v16, v12, vcc
	s_cselect_b64 vcc, -1, 0
	s_cmp_eq_u32 s0, 15
	v_cndmask_b32_e32 v16, v16, v13, vcc
	s_cselect_b64 vcc, -1, 0
	v_cndmask_b32_e32 v16, v16, v14, vcc
	v_cmp_ne_u32_e32 vcc, 0, v15
	s_add_i32 s0, 0, 0x24800
	s_nop 0
	v_cndmask_b32_e64 v15, 0, 1, vcc
	v_cmp_ne_u32_e32 vcc, 0, v0
	s_nop 1
	v_addc_co_u32_e32 v0, vcc, 0, v15, vcc
	v_cmp_ne_u32_e32 vcc, 0, v1
	s_nop 1
	v_cndmask_b32_e64 v1, 0, 1, vcc
	v_cmp_ne_u32_e32 vcc, 0, v2
	v_mov_b32_e32 v2, s0
	s_add_i32 s0, 0, 0x24804
	v_addc_co_u32_e32 v0, vcc, v0, v1, vcc
	v_cmp_ne_u32_e32 vcc, 0, v3
	s_nop 1
	v_cndmask_b32_e64 v1, 0, 1, vcc
	v_cmp_ne_u32_e32 vcc, 0, v4
	s_nop 1
	v_addc_co_u32_e32 v0, vcc, v0, v1, vcc
	v_cmp_ne_u32_e32 vcc, 0, v5
	s_nop 1
	v_cndmask_b32_e64 v1, 0, 1, vcc
	v_cmp_ne_u32_e32 vcc, 0, v6
	s_nop 1
	v_addc_co_u32_e32 v0, vcc, v0, v1, vcc
	v_cmp_ne_u32_e32 vcc, 0, v7
	s_nop 1
	v_cndmask_b32_e64 v1, 0, 1, vcc
	v_cmp_ne_u32_e32 vcc, 0, v8
	s_nop 1
	v_addc_co_u32_e32 v0, vcc, v0, v1, vcc
	v_cmp_ne_u32_e32 vcc, 0, v9
	s_nop 1
	v_cndmask_b32_e64 v1, 0, 1, vcc
	v_cmp_ne_u32_e32 vcc, 0, v10
	s_nop 1
	v_addc_co_u32_e32 v0, vcc, v0, v1, vcc
	v_cmp_ne_u32_e32 vcc, 0, v11
	s_nop 1
	v_cndmask_b32_e64 v1, 0, 1, vcc
	v_cmp_ne_u32_e32 vcc, 0, v12
	s_nop 1
	v_addc_co_u32_e32 v0, vcc, v0, v1, vcc
	v_cmp_ne_u32_e32 vcc, 0, v13
	s_nop 1
	v_cndmask_b32_e64 v1, 0, 1, vcc
	v_cmp_ne_u32_e32 vcc, 0, v14
	s_nop 1
	v_addc_co_u32_e32 v0, vcc, v0, v1, vcc
	v_max_u32_e32 v1, 1, v16
	v_max_u32_e32 v0, 1, v0
	ds_write_b32 v2, v1
	v_mov_b32_e32 v2, s0
	ds_write_b32 v2, v0
	s_branch .LBB0_107

.LBB0_225:
	v_readlane_b32 s3, v249, 34
	s_lshl_b32 s3, s3, 8
	s_waitcnt vmcnt(0)
	buffer_inv sc1
	s_waitcnt vmcnt(0)
	s_add_u32 s3, s94, s3
	s_addc_u32 s7, s95, 0
	s_add_u32 s6, s3, 0x2400
	s_addc_u32 s7, s7, 0
	s_mov_b64 s[10:11], -1
	s_mov_b64 s[8:9], exec
	v_mbcnt_lo_u32_b32 v0, s8, 0
	v_mbcnt_hi_u32_b32 v0, s9, v0
	v_cmp_eq_u32_e32 vcc, 0, v0
	s_and_b64 s[10:11], exec, vcc
	s_mov_b64 exec, s[10:11]
	s_cbranch_execz .LBB0_239
	s_bcnt1_i32_b64 s3, s[8:9]
	v_mov_b32_e32 v0, 0
	v_mov_b32_e32 v1, s3
	global_atomic_add v0, v1, s[6:7]
	s_branch .LBB0_239

.LBB0_381:
	s_cmp_gt_i32 s29, 3
	s_cselect_b64 s[4:5], -1, 0
	s_and_b64 s[0:1], s[6:7], s[4:5]
	s_andn2_b64 vcc, exec, s[0:1]
	s_cbranch_vccnz .LBB0_531
	s_waitcnt vmcnt(0)
	s_waitcnt lgkmcnt(0)
	s_barrier
	s_getreg_b32 s0, hwreg(HW_REG_HW_ID, 0, 6)
	s_lshl_b32 s0, s0, 2
	s_and_b32 s0, s0, 0xfc
	s_add_i32 s0, s0, 0
	s_add_i32 s0, s0, 0x25c00
	v_mov_b32_e32 v0, s0
	ds_read_b32 v0, v0
	s_waitcnt lgkmcnt(0)
	v_readfirstlane_b32 s0, v0
	v_mbcnt_lo_u32_b32 v0, -1, 0
	v_mbcnt_hi_u32_b32 v0, -1, v0
	s_nop 1
	v_lshl_add_u32 v0, s0, 6, v0
	s_nop 0
	v_cmp_eq_u32_e32 vcc, 0, v0
	s_and_saveexec_b64 s[6:7], vcc
	s_cbranch_execz .LBB0_410
	s_add_i32 s0, 0, 0x24800
	v_mov_b32_e32 v0, s0
	s_waitcnt vmcnt(0) expcnt(0) lgkmcnt(0)
	ds_read_b32 v1, v0
	s_add_i32 s0, 0, 0x24804
	v_mov_b32_e32 v0, s0
	ds_read_b32 v0, v0
	s_waitcnt lgkmcnt(1)
	v_cmp_ne_u32_e32 vcc, 0, v1
	s_cbranch_vccz .Lcensus_1

.LBB0_561:
	v_readlane_b32 s4, v249, 51
	v_readlane_b32 s5, v249, 52
	v_readlane_b32 s6, v249, 53
	v_readlane_b32 s7, v249, 54
	s_cmp_gt_i32 s5, 4
	s_cselect_b64 s[6:7], -1, 0
	s_and_b64 s[0:1], s[84:85], s[6:7]
	s_andn2_b64 vcc, exec, s[0:1]
	s_cbranch_vccnz .LBB0_711
	s_waitcnt vmcnt(0)
	s_waitcnt lgkmcnt(0)
	s_barrier
	s_getreg_b32 s0, hwreg(HW_REG_HW_ID, 0, 6)
	s_lshl_b32 s0, s0, 2
	s_and_b32 s0, s0, 0xfc
	s_add_i32 s0, s0, 0
	s_add_i32 s0, s0, 0x25c00
	v_mov_b32_e32 v0, s0
	ds_read_b32 v0, v0
	s_waitcnt lgkmcnt(0)
	v_readfirstlane_b32 s0, v0
	v_mbcnt_lo_u32_b32 v0, -1, 0
	v_mbcnt_hi_u32_b32 v0, -1, v0
	s_nop 1
	v_lshl_add_u32 v0, s0, 6, v0
	s_nop 0
	v_cmp_eq_u32_e32 vcc, 0, v0
	s_and_saveexec_b64 s[4:5], vcc
	s_cbranch_execz .LBB0_590
	s_add_i32 s0, 0, 0x24800
	v_mov_b32_e32 v0, s0
	s_waitcnt vmcnt(0) expcnt(0) lgkmcnt(0)
	ds_read_b32 v1, v0
	s_add_i32 s0, 0, 0x24804
	v_mov_b32_e32 v0, s0
	ds_read_b32 v0, v0
	s_waitcnt lgkmcnt(1)
	v_cmp_ne_u32_e32 vcc, 0, v1
	s_cbranch_vccz .Lcensus_2

.LBB0_696:
	v_readlane_b32 s3, v249, 34
	s_lshl_b32 s3, s3, 8
	s_waitcnt vmcnt(0)
	buffer_inv sc1
	s_waitcnt vmcnt(0)
	s_add_u32 s3, s94, s3
	s_addc_u32 s5, s95, 0
	s_add_u32 s4, s3, 0x2400
	s_addc_u32 s5, s5, 0
	s_mov_b64 s[10:11], -1
	s_mov_b64 s[8:9], exec
	v_mbcnt_lo_u32_b32 v0, s8, 0
	v_mbcnt_hi_u32_b32 v0, s9, v0
	v_cmp_eq_u32_e32 vcc, 0, v0
	s_and_b64 s[10:11], exec, vcc
	s_mov_b64 exec, s[10:11]
	s_cbranch_execz .LBB0_710
	s_bcnt1_i32_b64 s3, s[8:9]
	v_mov_b32_e32 v0, 0
	v_mov_b32_e32 v1, s3
	global_atomic_add v0, v1, s[4:5]
	s_branch .LBB0_710

.LBB0_732:
	s_cmp_gt_i32 s41, 5
	s_cselect_b64 s[12:13], -1, 0
	s_and_b64 s[0:1], s[8:9], s[12:13]
	s_andn2_b64 vcc, exec, s[0:1]
	s_cbranch_vccnz .LBB0_890
	s_waitcnt vmcnt(0)
	s_waitcnt lgkmcnt(0)
	s_barrier
	s_getreg_b32 s0, hwreg(HW_REG_HW_ID, 0, 6)
	s_lshl_b32 s0, s0, 2
	s_and_b32 s0, s0, 0xfc
	s_add_i32 s0, s0, 0
	s_add_i32 s0, s0, 0x25c00
	v_mov_b32_e32 v0, s0
	ds_read_b32 v0, v0
	s_waitcnt lgkmcnt(0)
	v_readfirstlane_b32 s0, v0
	v_mbcnt_lo_u32_b32 v0, -1, 0
	v_mbcnt_hi_u32_b32 v0, -1, v0
	s_nop 1
	v_lshl_add_u32 v0, s0, 6, v0
	s_nop 0
	v_cmp_eq_u32_e32 vcc, 0, v0
	s_and_saveexec_b64 s[6:7], vcc
	s_cbranch_execz .LBB0_761
	s_add_i32 s0, 0, 0x24800
	v_mov_b32_e32 v0, s0
	s_waitcnt vmcnt(0) expcnt(0) lgkmcnt(0)
	ds_read_b32 v1, v0
	s_add_i32 s0, 0, 0x24804
	v_mov_b32_e32 v0, s0
	ds_read_b32 v0, v0
	s_waitcnt lgkmcnt(1)
	v_cmp_ne_u32_e32 vcc, 0, v1
	s_cbranch_vccz .Lcensus_3

.Lcensus_3:
	v_readlane_b32 s0, v249, 0
	v_readlane_b32 s1, v249, 1
	s_load_dwordx2 s[10:11], s[0:1], 0x4
	s_add_u32 s0, s94, 0x1000
	s_addc_u32 s1, s95, 0
	s_add_u32 s8, s94, 0x1100
	s_addc_u32 s9, s95, 0
	s_waitcnt lgkmcnt(0)
	s_mul_i32 s3, s10, s33
	s_add_u32 s10, s94, 0x1200
	s_mul_i32 s3, s3, s11
	s_addc_u32 s11, s95, 0
	s_add_u32 s14, s94, 0x1300
	s_addc_u32 s15, s95, 0
	s_mov_b32 s22, 1
	v_mov_b32_e32 v16, 0
	s_branch .LBB0_737

.LBB0_923:
	s_cmp_gt_i32 s41, 6
	s_cselect_b64 s[4:5], -1, 0
	s_and_b64 s[0:1], s[14:15], s[4:5]
	s_andn2_b64 vcc, exec, s[0:1]
	s_cbranch_vccnz .LBB0_1075
	s_waitcnt vmcnt(0)
	s_waitcnt lgkmcnt(0)
	s_barrier
	s_getreg_b32 s0, hwreg(HW_REG_HW_ID, 0, 6)
	s_lshl_b32 s0, s0, 2
	s_and_b32 s0, s0, 0xfc
	s_add_i32 s0, s0, 0
	s_add_i32 s0, s0, 0x25c00
	v_mov_b32_e32 v0, s0
	ds_read_b32 v0, v0
	s_waitcnt lgkmcnt(0)
	v_readfirstlane_b32 s0, v0
	v_mbcnt_lo_u32_b32 v0, -1, 0
	v_mbcnt_hi_u32_b32 v0, -1, v0
	s_nop 1
	v_lshl_add_u32 v0, s0, 6, v0
	s_nop 0
	v_cmp_eq_u32_e32 vcc, 0, v0
	s_and_saveexec_b64 s[12:13], vcc
	s_cbranch_execz .LBB0_954
	s_add_i32 s0, 0, 0x24800
	v_mov_b32_e32 v0, s0
	s_waitcnt vmcnt(0) expcnt(0) lgkmcnt(0)
	ds_read_b32 v1, v0
	s_add_i32 s0, 0, 0x24804
	v_mov_b32_e32 v0, s0
	ds_read_b32 v0, v0
	s_waitcnt lgkmcnt(1)
	v_cmp_ne_u32_e32 vcc, 0, v1
	s_cbranch_vccz .Lcensus_4

.Lcensus_4:
	v_readlane_b32 s0, v249, 0
	v_readlane_b32 s1, v249, 1
	s_load_dwordx2 s[16:17], s[0:1], 0x4
	s_add_u32 s0, s94, 0x1000
	s_addc_u32 s1, s95, 0
	s_add_u32 s14, s94, 0x1100
	s_addc_u32 s15, s95, 0
	s_waitcnt lgkmcnt(0)
	s_mul_i32 s3, s16, s33
	s_add_u32 s16, s94, 0x1200
	s_mul_i32 s3, s3, s17
	s_addc_u32 s17, s95, 0
	s_add_u32 s18, s94, 0x1300
	s_addc_u32 s19, s95, 0
	s_mov_b32 s26, 1
	v_mov_b32_e32 v16, 0
	s_branch .LBB0_928

.LBB0_1060:
	v_readlane_b32 s3, v249, 34
	s_lshl_b32 s3, s3, 8
	s_waitcnt vmcnt(0)
	buffer_inv sc1
	s_waitcnt vmcnt(0)
	s_add_u32 s3, s94, s3
	s_addc_u32 s13, s95, 0
	s_add_u32 s12, s3, 0x2400
	s_addc_u32 s13, s13, 0
	s_mov_b64 s[16:17], -1
	s_mov_b64 s[14:15], exec
	v_mbcnt_lo_u32_b32 v0, s14, 0
	v_mbcnt_hi_u32_b32 v0, s15, v0
	v_cmp_eq_u32_e32 vcc, 0, v0
	s_and_b64 s[16:17], exec, vcc
	s_mov_b64 exec, s[16:17]
	s_cbranch_execz .LBB0_1074
	s_bcnt1_i32_b64 s3, s[14:15]
	v_mov_b32_e32 v0, 0
	v_mov_b32_e32 v1, s3
	global_atomic_add v0, v1, s[12:13]
	s_branch .LBB0_1074

.LBB0_1440:
	v_readlane_b32 s48, v249, 51
	v_readlane_b32 s49, v249, 52
	s_cmp_lt_i32 s48, 8
	s_cselect_b64 s[0:1], -1, 0
	s_cmp_gt_i32 s49, 8
	s_cselect_b64 s[4:5], -1, 0
	s_and_b64 s[0:1], s[0:1], s[4:5]
	s_andn2_b64 vcc, exec, s[0:1]
	v_readlane_b32 s50, v249, 53
	v_readlane_b32 s51, v249, 54
	s_cbranch_vccnz .LBB0_1590
	s_waitcnt vmcnt(0)
	s_waitcnt vmcnt(0) lgkmcnt(0)
	s_barrier
	s_getreg_b32 s0, hwreg(HW_REG_HW_ID, 0, 6)
	s_lshl_b32 s0, s0, 2
	s_and_b32 s0, s0, 0xfc
	s_add_i32 s0, s0, 0
	s_add_i32 s0, s0, 0x25c00
	v_mov_b32_e32 v0, s0
	ds_read_b32 v0, v0
	s_waitcnt lgkmcnt(0)
	v_readfirstlane_b32 s0, v0
	v_mbcnt_lo_u32_b32 v0, -1, 0
	v_mbcnt_hi_u32_b32 v0, -1, v0
	s_nop 1
	v_lshl_add_u32 v0, s0, 6, v0
	s_nop 0
	v_cmp_eq_u32_e32 vcc, 0, v0
	s_and_saveexec_b64 s[6:7], vcc
	s_cbranch_execz .LBB0_1469
	s_add_i32 s0, 0, 0x24800
	v_mov_b32_e32 v0, s0
	s_waitcnt vmcnt(0) expcnt(0) lgkmcnt(0)
	ds_read_b32 v1, v0
	s_add_i32 s0, 0, 0x24804
	v_mov_b32_e32 v0, s0
	ds_read_b32 v0, v0
	s_waitcnt lgkmcnt(1)
	v_cmp_ne_u32_e32 vcc, 0, v1
	s_cbranch_vccz .Lcensus_5

.Lcensus_5:
	v_readlane_b32 s0, v249, 0
	v_readlane_b32 s1, v249, 1
	s_load_dwordx2 s[12:13], s[0:1], 0x4
	s_add_u32 s0, s94, 0x1000
	s_addc_u32 s1, s95, 0
	s_add_u32 s10, s94, 0x1100
	s_addc_u32 s11, s95, 0
	s_waitcnt lgkmcnt(0)
	s_mul_i32 s3, s12, s33
	s_add_u32 s12, s94, 0x1200
	s_mul_i32 s3, s3, s13
	s_addc_u32 s13, s95, 0
	s_add_u32 s14, s94, 0x1300
	s_addc_u32 s15, s95, 0
	s_mov_b32 s22, 1
	v_mov_b32_e32 v16, 0
	s_branch .LBB0_1445

.LBB0_1575:
	v_readlane_b32 s3, v249, 34
	s_lshl_b32 s3, s3, 8
	s_waitcnt vmcnt(0)
	buffer_inv sc1
	s_waitcnt vmcnt(0)
	s_add_u32 s3, s94, s3
	s_addc_u32 s7, s95, 0
	s_add_u32 s6, s3, 0x2400
	s_addc_u32 s7, s7, 0
	s_mov_b64 s[12:13], -1
	s_mov_b64 s[10:11], exec
	v_mbcnt_lo_u32_b32 v0, s10, 0
	v_mbcnt_hi_u32_b32 v0, s11, v0
	v_cmp_eq_u32_e32 vcc, 0, v0
	s_and_b64 s[12:13], exec, vcc
	s_mov_b64 exec, s[12:13]
	s_cbranch_execz .LBB0_1589
	s_bcnt1_i32_b64 s3, s[10:11]
	v_mov_b32_e32 v0, 0
	v_mov_b32_e32 v1, s3
	global_atomic_add v0, v1, s[6:7]
	s_branch .LBB0_1589

.LBB0_1603:
	s_cmp_gt_i32 s49, 9
	s_cselect_b64 s[4:5], -1, 0
	s_and_b64 s[0:1], s[6:7], s[4:5]
	s_andn2_b64 vcc, exec, s[0:1]
	s_cbranch_vccnz .LBB0_1753
	s_waitcnt vmcnt(0)
	s_waitcnt vmcnt(0) lgkmcnt(0)
	s_barrier
	s_getreg_b32 s0, hwreg(HW_REG_HW_ID, 0, 6)
	s_lshl_b32 s0, s0, 2
	s_and_b32 s0, s0, 0xfc
	s_add_i32 s0, s0, 0
	s_add_i32 s0, s0, 0x25c00
	v_mov_b32_e32 v0, s0
	ds_read_b32 v0, v0
	s_waitcnt lgkmcnt(0)
	v_readfirstlane_b32 s0, v0
	v_mbcnt_lo_u32_b32 v0, -1, 0
	v_mbcnt_hi_u32_b32 v0, -1, v0
	s_nop 1
	v_lshl_add_u32 v0, s0, 6, v0
	s_nop 0
	v_cmp_eq_u32_e32 vcc, 0, v0
	s_and_saveexec_b64 s[6:7], vcc
	s_cbranch_execz .LBB0_1632
	s_add_i32 s0, 0, 0x24800
	v_mov_b32_e32 v0, s0
	s_waitcnt vmcnt(0) expcnt(0) lgkmcnt(0)
	ds_read_b32 v1, v0
	s_add_i32 s0, 0, 0x24804
	v_mov_b32_e32 v0, s0
	ds_read_b32 v0, v0
	s_waitcnt lgkmcnt(1)
	v_cmp_ne_u32_e32 vcc, 0, v1
	s_cbranch_vccz .Lcensus_6

.LBB0_1772:
	s_mov_b32 s5, 0
	v_mbcnt_lo_u32_b32 v147, -1, 0
	v_mbcnt_hi_u32_b32 v147, -1, v147
	s_lshl_b32 s5, s4, 8
	v_readlane_b32 s80, v249, 18
	v_bfe_u32 v58, v147, 4, 2
	v_lshlrev_b32_e32 v146, 3, v58
	v_or_b32_e32 v56, s41, v146
	v_or_b32_e32 v56, s5, v56
	v_ashrrev_i32_e32 v57, 31, v56
	v_readlane_b32 s90, v249, 28
	v_readlane_b32 s91, v249, 29
	v_cmp_eq_u32_e64 s[6:7], 0, v58
	s_add_i32 s51, s5, 0xfffff800
	v_lshl_add_u64 v[60:61], v[56:57], 2, s[90:91]
	global_load_dwordx4 v[76:79], v[60:61], off
	global_load_dwordx4 v[68:71], v[60:61], off offset:16
	global_load_dwordx4 v[56:59], v[60:61], off offset:528
	s_nop 0
	global_load_dwordx4 v[60:63], v[60:61], off offset:512
	s_cmp_gt_i32 s4, 7
	v_readlane_b32 s81, v249, 19
	v_readlane_b32 s82, v249, 20
	v_readlane_b32 s83, v249, 21
	v_readlane_b32 s84, v249, 22
	v_readlane_b32 s85, v249, 23
	v_readlane_b32 s86, v249, 24
	v_readlane_b32 s87, v249, 25
	s_cselect_b64 s[70:71], -1, 0
	s_and_b64 s[72:73], s[70:71], exec
	s_mov_b32 s53, 0x16500000
	v_readlane_b32 s80, v249, 55
	s_cselect_b32 s53, s53, 0x12500000
	v_readlane_b32 s86, v249, 61
	s_cselect_b32 s5, s51, s5
	v_readlane_b32 s87, v249, 62
	s_add_u32 s72, s86, s53
	s_addc_u32 s73, s87, 0
	s_lshl_b32 s51, s68, 8
	s_or_b32 s5, s41, s5
	s_add_i32 s51, s51, s39
	v_or_b32_e32 v146, s5, v146
	v_and_or_b32 v148, v147, 15, s51
	v_ashrrev_i32_e32 v147, 31, v146
	v_ashrrev_i32_e32 v149, 31, v148
	v_lshl_add_u64 v[146:147], v[146:147], 1, s[72:73]
	v_lshlrev_b64 v[160:161], 12, v[148:149]
	v_lshl_add_u64 v[164:165], v[146:147], 0, v[160:161]
	v_mov_b64_e32 v[150:151], s[24:25]
	s_lshl_b32 s53, s4, 2
	s_sub_i32 s68, s53, 32
	s_ashr_i32 s69, s68, 31
	s_or_b64 s[68:69], s[68:69], s[14:15]
	s_cmp_lt_i32 s4, 8
	v_readlane_b32 s88, v249, 26
	v_readlane_b32 s89, v249, 27
	v_readlane_b32 s92, v249, 30
	v_readlane_b32 s93, v249, 31
	v_readlane_b32 s94, v249, 32
	v_readlane_b32 s95, v249, 33
	v_readlane_b32 s81, v249, 56
	v_readlane_b32 s82, v249, 57
	v_readlane_b32 s83, v249, 58
	v_readlane_b32 s84, v249, 59
	v_readlane_b32 s85, v249, 60
	s_waitcnt vmcnt(0)
	v_readlane_b32 s90, v249, 63
	v_readlane_b32 s91, v248, 0
	s_mov_b64 s[94:95], s[46:47]
	v_mov_b32_e32 v192, v148
	v_ashrrev_i32_e32 v193, 31, v192
	v_lshlrev_b64 v[194:195], 12, v[192:193]
	v_lshl_add_u64 v[196:197], v[146:147], 0, v[194:195]
	v_pk_add_f32 v[140:141], v[140:141], v[76:77]
	v_pk_add_f32 v[142:143], v[142:143], v[78:79]
	v_pk_add_f32 v[136:137], v[136:137], v[68:69]
	v_pk_add_f32 v[138:139], v[138:139], v[70:71]
	v_med3_f32 v160, v140, s78, v158
	v_med3_f32 v161, v141, s78, v158
	v_med3_f32 v162, v142, s78, v158
	v_med3_f32 v163, v143, s78, v158
	v_med3_f32 v164, v136, s78, v158
	v_med3_f32 v165, v137, s78, v158
	v_med3_f32 v166, v138, s78, v158
	v_med3_f32 v167, v139, s78, v158
	v_pk_mul_f32 v[168:169], v[160:161], v[160:161]
	v_pk_mul_f32 v[170:171], v[162:163], v[162:163]
	v_pk_mul_f32 v[172:173], v[164:165], v[164:165]
	v_pk_mul_f32 v[174:175], v[166:167], v[166:167]
	v_pk_fma_f32 v[168:169], v[168:169], s[20:21], -1.0 op_sel_hi:[1,0,0]
	v_pk_fma_f32 v[170:171], v[170:171], s[20:21], -1.0 op_sel_hi:[1,0,0]
	v_pk_fma_f32 v[172:173], v[172:173], s[20:21], -1.0 op_sel_hi:[1,0,0]
	v_pk_fma_f32 v[174:175], v[174:175], s[20:21], -1.0 op_sel_hi:[1,0,0]
	v_pk_fma_f32 v[176:177], v[168:169], s[22:23], v[150:151] op_sel_hi:[1,0,0] neg_lo:[1,0,0] neg_hi:[1,0,0]
	v_pk_fma_f32 v[178:179], v[170:171], s[22:23], v[150:151] op_sel_hi:[1,0,0] neg_lo:[1,0,0] neg_hi:[1,0,0]
	v_pk_fma_f32 v[180:181], v[172:173], s[22:23], v[150:151] op_sel_hi:[1,0,0] neg_lo:[1,0,0] neg_hi:[1,0,0]
	v_pk_fma_f32 v[182:183], v[174:175], s[22:23], v[150:151] op_sel_hi:[1,0,0] neg_lo:[1,0,0] neg_hi:[1,0,0]
	v_pk_fma_f32 v[176:177], v[168:169], v[176:177], s[26:27] op_sel_hi:[1,1,0]
	v_pk_fma_f32 v[178:179], v[170:171], v[178:179], s[26:27] op_sel_hi:[1,1,0]
	v_pk_fma_f32 v[180:181], v[172:173], v[180:181], s[26:27] op_sel_hi:[1,1,0]
	v_pk_fma_f32 v[182:183], v[174:175], v[182:183], s[26:27] op_sel_hi:[1,1,0]
	v_pk_fma_f32 v[176:177], v[168:169], v[176:177], s[28:29] op_sel_hi:[1,1,0]
	v_pk_fma_f32 v[178:179], v[170:171], v[178:179], s[28:29] op_sel_hi:[1,1,0]
	v_pk_fma_f32 v[180:181], v[172:173], v[180:181], s[28:29] op_sel_hi:[1,1,0]
	v_pk_fma_f32 v[182:183], v[174:175], v[182:183], s[28:29] op_sel_hi:[1,1,0]
	v_pk_fma_f32 v[176:177], v[168:169], v[176:177], s[30:31] op_sel_hi:[1,1,0]
	v_pk_fma_f32 v[178:179], v[170:171], v[178:179], s[30:31] op_sel_hi:[1,1,0]
	v_pk_fma_f32 v[180:181], v[172:173], v[180:181], s[30:31] op_sel_hi:[1,1,0]
	v_pk_fma_f32 v[182:183], v[174:175], v[182:183], s[30:31] op_sel_hi:[1,1,0]
	v_pk_fma_f32 v[176:177], v[168:169], v[176:177], s[34:35] op_sel_hi:[1,1,0]
	v_pk_fma_f32 v[178:179], v[170:171], v[178:179], s[34:35] op_sel_hi:[1,1,0]
	v_pk_fma_f32 v[180:181], v[172:173], v[180:181], s[34:35] op_sel_hi:[1,1,0]
	v_pk_fma_f32 v[182:183], v[174:175], v[182:183], s[34:35] op_sel_hi:[1,1,0]
	v_pk_fma_f32 v[176:177], v[168:169], v[176:177], s[36:37] op_sel_hi:[1,1,0]
	v_pk_fma_f32 v[178:179], v[170:171], v[178:179], s[36:37] op_sel_hi:[1,1,0]
	v_pk_fma_f32 v[180:181], v[172:173], v[180:181], s[36:37] op_sel_hi:[1,1,0]
	v_pk_fma_f32 v[182:183], v[174:175], v[182:183], s[36:37] op_sel_hi:[1,1,0]
	v_pk_fma_f32 v[176:177], v[168:169], v[176:177], s[38:39] op_sel_hi:[1,1,0]
	v_pk_fma_f32 v[178:179], v[170:171], v[178:179], s[38:39] op_sel_hi:[1,1,0]
	v_pk_fma_f32 v[180:181], v[172:173], v[180:181], s[38:39] op_sel_hi:[1,1,0]
	v_pk_fma_f32 v[182:183], v[174:175], v[182:183], s[38:39] op_sel_hi:[1,1,0]
	v_pk_fma_f32 v[176:177], v[168:169], v[176:177], s[40:41] op_sel_hi:[1,1,0]
	v_pk_fma_f32 v[178:179], v[170:171], v[178:179], s[40:41] op_sel_hi:[1,1,0]
	v_pk_fma_f32 v[180:181], v[172:173], v[180:181], s[40:41] op_sel_hi:[1,1,0]
	v_pk_fma_f32 v[182:183], v[174:175], v[182:183], s[40:41] op_sel_hi:[1,1,0]
	v_pk_fma_f32 v[176:177], v[168:169], v[176:177], s[42:43] op_sel_hi:[1,1,0]
	v_pk_fma_f32 v[178:179], v[170:171], v[178:179], s[42:43] op_sel_hi:[1,1,0]
	v_pk_fma_f32 v[180:181], v[172:173], v[180:181], s[42:43] op_sel_hi:[1,1,0]
	v_pk_fma_f32 v[182:183], v[174:175], v[182:183], s[42:43] op_sel_hi:[1,1,0]
	v_pk_fma_f32 v[176:177], v[168:169], v[176:177], s[44:45] op_sel_hi:[1,1,0]
	v_pk_fma_f32 v[178:179], v[170:171], v[178:179], s[44:45] op_sel_hi:[1,1,0]
	v_pk_fma_f32 v[180:181], v[172:173], v[180:181], s[44:45] op_sel_hi:[1,1,0]
	v_pk_fma_f32 v[182:183], v[174:175], v[182:183], s[44:45] op_sel_hi:[1,1,0]
	v_pk_fma_f32 v[168:169], v[168:169], v[176:177], s[48:49] op_sel_hi:[1,1,0]
	v_pk_fma_f32 v[170:171], v[170:171], v[178:179], s[48:49] op_sel_hi:[1,1,0]
	v_pk_fma_f32 v[172:173], v[172:173], v[180:181], s[48:49] op_sel_hi:[1,1,0]
	v_pk_fma_f32 v[174:175], v[174:175], v[182:183], s[48:49] op_sel_hi:[1,1,0]
	v_pk_fma_f32 v[160:161], v[160:161], v[168:169], 0.5 op_sel_hi:[1,1,0]
	v_pk_fma_f32 v[162:163], v[162:163], v[170:171], 0.5 op_sel_hi:[1,1,0]
	v_pk_fma_f32 v[164:165], v[164:165], v[172:173], 0.5 op_sel_hi:[1,1,0]
	v_pk_fma_f32 v[166:167], v[166:167], v[174:175], 0.5 op_sel_hi:[1,1,0]
	v_pk_mul_f32 v[140:141], v[140:141], v[160:161]
	v_pk_mul_f32 v[142:143], v[142:143], v[162:163]
	v_pk_mul_f32 v[136:137], v[136:137], v[164:165]
	v_pk_mul_f32 v[138:139], v[138:139], v[166:167]
	v_cvt_pk_bf16_f32 v184, v140, v141
	v_cvt_pk_bf16_f32 v185, v142, v143
	v_cvt_pk_bf16_f32 v186, v136, v137
	v_cvt_pk_bf16_f32 v187, v138, v139
	global_store_dwordx4 v[196:197], v[184:187], off
	v_pk_add_f32 v[132:133], v[132:133], v[60:61]
	v_pk_add_f32 v[134:135], v[134:135], v[62:63]
	v_pk_add_f32 v[128:129], v[128:129], v[56:57]
	v_pk_add_f32 v[130:131], v[130:131], v[58:59]
	v_med3_f32 v160, v132, s78, v158
	v_med3_f32 v161, v133, s78, v158
	v_med3_f32 v162, v134, s78, v158
	v_med3_f32 v163, v135, s78, v158
	v_med3_f32 v164, v128, s78, v158
	v_med3_f32 v165, v129, s78, v158
	v_med3_f32 v166, v130, s78, v158
	v_med3_f32 v167, v131, s78, v158
	v_pk_mul_f32 v[168:169], v[160:161], v[160:161]
	v_pk_mul_f32 v[170:171], v[162:163], v[162:163]
	v_pk_mul_f32 v[172:173], v[164:165], v[164:165]
	v_pk_mul_f32 v[174:175], v[166:167], v[166:167]
	v_pk_fma_f32 v[168:169], v[168:169], s[20:21], -1.0 op_sel_hi:[1,0,0]
	v_pk_fma_f32 v[170:171], v[170:171], s[20:21], -1.0 op_sel_hi:[1,0,0]
	v_pk_fma_f32 v[172:173], v[172:173], s[20:21], -1.0 op_sel_hi:[1,0,0]
	v_pk_fma_f32 v[174:175], v[174:175], s[20:21], -1.0 op_sel_hi:[1,0,0]
	v_pk_fma_f32 v[176:177], v[168:169], s[22:23], v[150:151] op_sel_hi:[1,0,0] neg_lo:[1,0,0] neg_hi:[1,0,0]
	v_pk_fma_f32 v[178:179], v[170:171], s[22:23], v[150:151] op_sel_hi:[1,0,0] neg_lo:[1,0,0] neg_hi:[1,0,0]
	v_pk_fma_f32 v[180:181], v[172:173], s[22:23], v[150:151] op_sel_hi:[1,0,0] neg_lo:[1,0,0] neg_hi:[1,0,0]
	v_pk_fma_f32 v[182:183], v[174:175], s[22:23], v[150:151] op_sel_hi:[1,0,0] neg_lo:[1,0,0] neg_hi:[1,0,0]
	v_pk_fma_f32 v[176:177], v[168:169], v[176:177], s[26:27] op_sel_hi:[1,1,0]
	v_pk_fma_f32 v[178:179], v[170:171], v[178:179], s[26:27] op_sel_hi:[1,1,0]
	v_pk_fma_f32 v[180:181], v[172:173], v[180:181], s[26:27] op_sel_hi:[1,1,0]
	v_pk_fma_f32 v[182:183], v[174:175], v[182:183], s[26:27] op_sel_hi:[1,1,0]
	v_pk_fma_f32 v[176:177], v[168:169], v[176:177], s[28:29] op_sel_hi:[1,1,0]
	v_pk_fma_f32 v[178:179], v[170:171], v[178:179], s[28:29] op_sel_hi:[1,1,0]
	v_pk_fma_f32 v[180:181], v[172:173], v[180:181], s[28:29] op_sel_hi:[1,1,0]
	v_pk_fma_f32 v[182:183], v[174:175], v[182:183], s[28:29] op_sel_hi:[1,1,0]
	v_pk_fma_f32 v[176:177], v[168:169], v[176:177], s[30:31] op_sel_hi:[1,1,0]
	v_pk_fma_f32 v[178:179], v[170:171], v[178:179], s[30:31] op_sel_hi:[1,1,0]
	v_pk_fma_f32 v[180:181], v[172:173], v[180:181], s[30:31] op_sel_hi:[1,1,0]
	v_pk_fma_f32 v[182:183], v[174:175], v[182:183], s[30:31] op_sel_hi:[1,1,0]
	v_pk_fma_f32 v[176:177], v[168:169], v[176:177], s[34:35] op_sel_hi:[1,1,0]
	v_pk_fma_f32 v[178:179], v[170:171], v[178:179], s[34:35] op_sel_hi:[1,1,0]
	v_pk_fma_f32 v[180:181], v[172:173], v[180:181], s[34:35] op_sel_hi:[1,1,0]
	v_pk_fma_f32 v[182:183], v[174:175], v[182:183], s[34:35] op_sel_hi:[1,1,0]
	v_pk_fma_f32 v[176:177], v[168:169], v[176:177], s[36:37] op_sel_hi:[1,1,0]
	v_pk_fma_f32 v[178:179], v[170:171], v[178:179], s[36:37] op_sel_hi:[1,1,0]
	v_pk_fma_f32 v[180:181], v[172:173], v[180:181], s[36:37] op_sel_hi:[1,1,0]
	v_pk_fma_f32 v[182:183], v[174:175], v[182:183], s[36:37] op_sel_hi:[1,1,0]
	v_pk_fma_f32 v[176:177], v[168:169], v[176:177], s[38:39] op_sel_hi:[1,1,0]
	v_pk_fma_f32 v[178:179], v[170:171], v[178:179], s[38:39] op_sel_hi:[1,1,0]
	v_pk_fma_f32 v[180:181], v[172:173], v[180:181], s[38:39] op_sel_hi:[1,1,0]
	v_pk_fma_f32 v[182:183], v[174:175], v[182:183], s[38:39] op_sel_hi:[1,1,0]
	v_pk_fma_f32 v[176:177], v[168:169], v[176:177], s[40:41] op_sel_hi:[1,1,0]
	v_pk_fma_f32 v[178:179], v[170:171], v[178:179], s[40:41] op_sel_hi:[1,1,0]
	v_pk_fma_f32 v[180:181], v[172:173], v[180:181], s[40:41] op_sel_hi:[1,1,0]
	v_pk_fma_f32 v[182:183], v[174:175], v[182:183], s[40:41] op_sel_hi:[1,1,0]
	v_pk_fma_f32 v[176:177], v[168:169], v[176:177], s[42:43] op_sel_hi:[1,1,0]
	v_pk_fma_f32 v[178:179], v[170:171], v[178:179], s[42:43] op_sel_hi:[1,1,0]
	v_pk_fma_f32 v[180:181], v[172:173], v[180:181], s[42:43] op_sel_hi:[1,1,0]
	v_pk_fma_f32 v[182:183], v[174:175], v[182:183], s[42:43] op_sel_hi:[1,1,0]
	v_pk_fma_f32 v[176:177], v[168:169], v[176:177], s[44:45] op_sel_hi:[1,1,0]
	v_pk_fma_f32 v[178:179], v[170:171], v[178:179], s[44:45] op_sel_hi:[1,1,0]
	v_pk_fma_f32 v[180:181], v[172:173], v[180:181], s[44:45] op_sel_hi:[1,1,0]
	v_pk_fma_f32 v[182:183], v[174:175], v[182:183], s[44:45] op_sel_hi:[1,1,0]
	v_pk_fma_f32 v[168:169], v[168:169], v[176:177], s[48:49] op_sel_hi:[1,1,0]
	v_pk_fma_f32 v[170:171], v[170:171], v[178:179], s[48:49] op_sel_hi:[1,1,0]
	v_pk_fma_f32 v[172:173], v[172:173], v[180:181], s[48:49] op_sel_hi:[1,1,0]
	v_pk_fma_f32 v[174:175], v[174:175], v[182:183], s[48:49] op_sel_hi:[1,1,0]
	v_pk_fma_f32 v[160:161], v[160:161], v[168:169], 0.5 op_sel_hi:[1,1,0]
	v_pk_fma_f32 v[162:163], v[162:163], v[170:171], 0.5 op_sel_hi:[1,1,0]
	v_pk_fma_f32 v[164:165], v[164:165], v[172:173], 0.5 op_sel_hi:[1,1,0]
	v_pk_fma_f32 v[166:167], v[166:167], v[174:175], 0.5 op_sel_hi:[1,1,0]
	v_pk_mul_f32 v[132:133], v[132:133], v[160:161]
	v_pk_mul_f32 v[134:135], v[134:135], v[162:163]
	v_pk_mul_f32 v[128:129], v[128:129], v[164:165]
	v_pk_mul_f32 v[130:131], v[130:131], v[166:167]
	v_cvt_pk_bf16_f32 v188, v132, v133
	v_cvt_pk_bf16_f32 v189, v134, v135
	v_cvt_pk_bf16_f32 v190, v128, v129
	v_cvt_pk_bf16_f32 v191, v130, v131
	global_store_dwordx4 v[196:197], v[188:191], off offset:256
	s_and_b64 vcc, exec, s[70:71]
	s_cbranch_vccz .Lg9_nostat_0
	v_pk_add_f32 v[160:161], v[140:141], v[142:143]
	v_pk_add_f32 v[162:163], v[136:137], v[138:139]
	v_pk_add_f32 v[164:165], v[132:133], v[134:135]
	v_pk_add_f32 v[166:167], v[128:129], v[130:131]
	v_pk_mul_f32 v[168:169], v[140:141], v[140:141]
	v_pk_mul_f32 v[170:171], v[132:133], v[132:133]
	v_pk_add_f32 v[160:161], v[160:161], v[162:163]
	v_pk_add_f32 v[164:165], v[164:165], v[166:167]
	v_pk_fma_f32 v[168:169], v[142:143], v[142:143], v[168:169]
	v_pk_fma_f32 v[170:171], v[134:135], v[134:135], v[170:171]
	v_pk_fma_f32 v[168:169], v[136:137], v[136:137], v[168:169]
	v_pk_fma_f32 v[170:171], v[128:129], v[128:129], v[170:171]
	v_pk_fma_f32 v[168:169], v[138:139], v[138:139], v[168:169]
	v_pk_fma_f32 v[170:171], v[130:131], v[130:131], v[170:171]
	v_pk_add_f32 v[160:161], v[160:161], v[164:165]
	v_pk_add_f32 v[168:169], v[168:169], v[170:171]
	s_nop 0
	v_add_f32_e32 v198, v160, v161
	v_add_f32_e32 v200, v168, v169
	v_mov_b32_e32 v199, v198
	s_nop 1
	v_permlane16_swap_b32 v199, v198
	s_nop 1
	v_add_f32_e32 v198, v199, v198
	v_mov_b32_e32 v202, v198
	v_mov_b32_e32 v201, v200
	s_nop 1
	v_permlane32_swap_b32 v202, v198
	s_nop 1
	s_nop 1
	v_permlane16_swap_b32 v201, v200
	s_nop 1
	v_add_f32_e32 v199, v201, v200
	v_mov_b32_e32 v203, v199
	s_nop 1
	v_permlane32_swap_b32 v203, v199
	s_nop 1
	s_and_saveexec_b64 s[4:5], s[6:7]
	v_lshlrev_b64 v[194:195], 8, v[192:193]
	v_lshl_add_u64 v[194:195], s[16:17], 0, v[194:195]
	v_lshl_add_u64 v[194:195], s[68:69], 3, v[194:195]
	v_pk_add_f32 v[200:201], v[202:203], v[198:199]
	global_store_dwordx2 v[194:195], v[200:201], off
	s_or_b64 exec, exec, s[4:5]
.Lg9_nostat_0:
	v_add_u32_e32 v192, 0x10, v148
	v_ashrrev_i32_e32 v193, 31, v192
	v_lshlrev_b64 v[194:195], 12, v[192:193]
	v_lshl_add_u64 v[196:197], v[146:147], 0, v[194:195]
	v_pk_add_f32 v[124:125], v[124:125], v[76:77]
	v_pk_add_f32 v[126:127], v[126:127], v[78:79]
	v_pk_add_f32 v[120:121], v[120:121], v[68:69]
	v_pk_add_f32 v[122:123], v[122:123], v[70:71]
	v_med3_f32 v160, v124, s78, v158
	v_med3_f32 v161, v125, s78, v158
	v_med3_f32 v162, v126, s78, v158
	v_med3_f32 v163, v127, s78, v158
	v_med3_f32 v164, v120, s78, v158
	v_med3_f32 v165, v121, s78, v158
	v_med3_f32 v166, v122, s78, v158
	v_med3_f32 v167, v123, s78, v158
	v_pk_mul_f32 v[168:169], v[160:161], v[160:161]
	v_pk_mul_f32 v[170:171], v[162:163], v[162:163]
	v_pk_mul_f32 v[172:173], v[164:165], v[164:165]
	v_pk_mul_f32 v[174:175], v[166:167], v[166:167]
	v_pk_fma_f32 v[168:169], v[168:169], s[20:21], -1.0 op_sel_hi:[1,0,0]
	v_pk_fma_f32 v[170:171], v[170:171], s[20:21], -1.0 op_sel_hi:[1,0,0]
	v_pk_fma_f32 v[172:173], v[172:173], s[20:21], -1.0 op_sel_hi:[1,0,0]
	v_pk_fma_f32 v[174:175], v[174:175], s[20:21], -1.0 op_sel_hi:[1,0,0]
	v_pk_fma_f32 v[176:177], v[168:169], s[22:23], v[150:151] op_sel_hi:[1,0,0] neg_lo:[1,0,0] neg_hi:[1,0,0]
	v_pk_fma_f32 v[178:179], v[170:171], s[22:23], v[150:151] op_sel_hi:[1,0,0] neg_lo:[1,0,0] neg_hi:[1,0,0]
	v_pk_fma_f32 v[180:181], v[172:173], s[22:23], v[150:151] op_sel_hi:[1,0,0] neg_lo:[1,0,0] neg_hi:[1,0,0]
	v_pk_fma_f32 v[182:183], v[174:175], s[22:23], v[150:151] op_sel_hi:[1,0,0] neg_lo:[1,0,0] neg_hi:[1,0,0]
	v_pk_fma_f32 v[176:177], v[168:169], v[176:177], s[26:27] op_sel_hi:[1,1,0]
	v_pk_fma_f32 v[178:179], v[170:171], v[178:179], s[26:27] op_sel_hi:[1,1,0]
	v_pk_fma_f32 v[180:181], v[172:173], v[180:181], s[26:27] op_sel_hi:[1,1,0]
	v_pk_fma_f32 v[182:183], v[174:175], v[182:183], s[26:27] op_sel_hi:[1,1,0]
	v_pk_fma_f32 v[176:177], v[168:169], v[176:177], s[28:29] op_sel_hi:[1,1,0]
	v_pk_fma_f32 v[178:179], v[170:171], v[178:179], s[28:29] op_sel_hi:[1,1,0]
	v_pk_fma_f32 v[180:181], v[172:173], v[180:181], s[28:29] op_sel_hi:[1,1,0]
	v_pk_fma_f32 v[182:183], v[174:175], v[182:183], s[28:29] op_sel_hi:[1,1,0]
	v_pk_fma_f32 v[176:177], v[168:169], v[176:177], s[30:31] op_sel_hi:[1,1,0]
	v_pk_fma_f32 v[178:179], v[170:171], v[178:179], s[30:31] op_sel_hi:[1,1,0]
	v_pk_fma_f32 v[180:181], v[172:173], v[180:181], s[30:31] op_sel_hi:[1,1,0]
	v_pk_fma_f32 v[182:183], v[174:175], v[182:183], s[30:31] op_sel_hi:[1,1,0]
	v_pk_fma_f32 v[176:177], v[168:169], v[176:177], s[34:35] op_sel_hi:[1,1,0]
	v_pk_fma_f32 v[178:179], v[170:171], v[178:179], s[34:35] op_sel_hi:[1,1,0]
	v_pk_fma_f32 v[180:181], v[172:173], v[180:181], s[34:35] op_sel_hi:[1,1,0]
	v_pk_fma_f32 v[182:183], v[174:175], v[182:183], s[34:35] op_sel_hi:[1,1,0]
	v_pk_fma_f32 v[176:177], v[168:169], v[176:177], s[36:37] op_sel_hi:[1,1,0]
	v_pk_fma_f32 v[178:179], v[170:171], v[178:179], s[36:37] op_sel_hi:[1,1,0]
	v_pk_fma_f32 v[180:181], v[172:173], v[180:181], s[36:37] op_sel_hi:[1,1,0]
	v_pk_fma_f32 v[182:183], v[174:175], v[182:183], s[36:37] op_sel_hi:[1,1,0]
	v_pk_fma_f32 v[176:177], v[168:169], v[176:177], s[38:39] op_sel_hi:[1,1,0]
	v_pk_fma_f32 v[178:179], v[170:171], v[178:179], s[38:39] op_sel_hi:[1,1,0]
	v_pk_fma_f32 v[180:181], v[172:173], v[180:181], s[38:39] op_sel_hi:[1,1,0]
	v_pk_fma_f32 v[182:183], v[174:175], v[182:183], s[38:39] op_sel_hi:[1,1,0]
	v_pk_fma_f32 v[176:177], v[168:169], v[176:177], s[40:41] op_sel_hi:[1,1,0]
	v_pk_fma_f32 v[178:179], v[170:171], v[178:179], s[40:41] op_sel_hi:[1,1,0]
	v_pk_fma_f32 v[180:181], v[172:173], v[180:181], s[40:41] op_sel_hi:[1,1,0]
	v_pk_fma_f32 v[182:183], v[174:175], v[182:183], s[40:41] op_sel_hi:[1,1,0]
	v_pk_fma_f32 v[176:177], v[168:169], v[176:177], s[42:43] op_sel_hi:[1,1,0]
	v_pk_fma_f32 v[178:179], v[170:171], v[178:179], s[42:43] op_sel_hi:[1,1,0]
	v_pk_fma_f32 v[180:181], v[172:173], v[180:181], s[42:43] op_sel_hi:[1,1,0]
	v_pk_fma_f32 v[182:183], v[174:175], v[182:183], s[42:43] op_sel_hi:[1,1,0]
	v_pk_fma_f32 v[176:177], v[168:169], v[176:177], s[44:45] op_sel_hi:[1,1,0]
	v_pk_fma_f32 v[178:179], v[170:171], v[178:179], s[44:45] op_sel_hi:[1,1,0]
	v_pk_fma_f32 v[180:181], v[172:173], v[180:181], s[44:45] op_sel_hi:[1,1,0]
	v_pk_fma_f32 v[182:183], v[174:175], v[182:183], s[44:45] op_sel_hi:[1,1,0]
	v_pk_fma_f32 v[168:169], v[168:169], v[176:177], s[48:49] op_sel_hi:[1,1,0]
	v_pk_fma_f32 v[170:171], v[170:171], v[178:179], s[48:49] op_sel_hi:[1,1,0]
	v_pk_fma_f32 v[172:173], v[172:173], v[180:181], s[48:49] op_sel_hi:[1,1,0]
	v_pk_fma_f32 v[174:175], v[174:175], v[182:183], s[48:49] op_sel_hi:[1,1,0]
	v_pk_fma_f32 v[160:161], v[160:161], v[168:169], 0.5 op_sel_hi:[1,1,0]
	v_pk_fma_f32 v[162:163], v[162:163], v[170:171], 0.5 op_sel_hi:[1,1,0]
	v_pk_fma_f32 v[164:165], v[164:165], v[172:173], 0.5 op_sel_hi:[1,1,0]
	v_pk_fma_f32 v[166:167], v[166:167], v[174:175], 0.5 op_sel_hi:[1,1,0]
	v_pk_mul_f32 v[124:125], v[124:125], v[160:161]
	v_pk_mul_f32 v[126:127], v[126:127], v[162:163]
	v_pk_mul_f32 v[120:121], v[120:121], v[164:165]
	v_pk_mul_f32 v[122:123], v[122:123], v[166:167]
	v_cvt_pk_bf16_f32 v184, v124, v125
	v_cvt_pk_bf16_f32 v185, v126, v127
	v_cvt_pk_bf16_f32 v186, v120, v121
	v_cvt_pk_bf16_f32 v187, v122, v123
	global_store_dwordx4 v[196:197], v[184:187], off
	v_pk_add_f32 v[116:117], v[116:117], v[60:61]
	v_pk_add_f32 v[118:119], v[118:119], v[62:63]
	v_pk_add_f32 v[112:113], v[112:113], v[56:57]
	v_pk_add_f32 v[114:115], v[114:115], v[58:59]
	v_med3_f32 v160, v116, s78, v158
	v_med3_f32 v161, v117, s78, v158
	v_med3_f32 v162, v118, s78, v158
	v_med3_f32 v163, v119, s78, v158
	v_med3_f32 v164, v112, s78, v158
	v_med3_f32 v165, v113, s78, v158
	v_med3_f32 v166, v114, s78, v158
	v_med3_f32 v167, v115, s78, v158
	v_pk_mul_f32 v[168:169], v[160:161], v[160:161]
	v_pk_mul_f32 v[170:171], v[162:163], v[162:163]
	v_pk_mul_f32 v[172:173], v[164:165], v[164:165]
	v_pk_mul_f32 v[174:175], v[166:167], v[166:167]
	v_pk_fma_f32 v[168:169], v[168:169], s[20:21], -1.0 op_sel_hi:[1,0,0]
	v_pk_fma_f32 v[170:171], v[170:171], s[20:21], -1.0 op_sel_hi:[1,0,0]
	v_pk_fma_f32 v[172:173], v[172:173], s[20:21], -1.0 op_sel_hi:[1,0,0]
	v_pk_fma_f32 v[174:175], v[174:175], s[20:21], -1.0 op_sel_hi:[1,0,0]
	v_pk_fma_f32 v[176:177], v[168:169], s[22:23], v[150:151] op_sel_hi:[1,0,0] neg_lo:[1,0,0] neg_hi:[1,0,0]
	v_pk_fma_f32 v[178:179], v[170:171], s[22:23], v[150:151] op_sel_hi:[1,0,0] neg_lo:[1,0,0] neg_hi:[1,0,0]
	v_pk_fma_f32 v[180:181], v[172:173], s[22:23], v[150:151] op_sel_hi:[1,0,0] neg_lo:[1,0,0] neg_hi:[1,0,0]
	v_pk_fma_f32 v[182:183], v[174:175], s[22:23], v[150:151] op_sel_hi:[1,0,0] neg_lo:[1,0,0] neg_hi:[1,0,0]
	v_pk_fma_f32 v[176:177], v[168:169], v[176:177], s[26:27] op_sel_hi:[1,1,0]
	v_pk_fma_f32 v[178:179], v[170:171], v[178:179], s[26:27] op_sel_hi:[1,1,0]
	v_pk_fma_f32 v[180:181], v[172:173], v[180:181], s[26:27] op_sel_hi:[1,1,0]
	v_pk_fma_f32 v[182:183], v[174:175], v[182:183], s[26:27] op_sel_hi:[1,1,0]
	v_pk_fma_f32 v[176:177], v[168:169], v[176:177], s[28:29] op_sel_hi:[1,1,0]
	v_pk_fma_f32 v[178:179], v[170:171], v[178:179], s[28:29] op_sel_hi:[1,1,0]
	v_pk_fma_f32 v[180:181], v[172:173], v[180:181], s[28:29] op_sel_hi:[1,1,0]
	v_pk_fma_f32 v[182:183], v[174:175], v[182:183], s[28:29] op_sel_hi:[1,1,0]
	v_pk_fma_f32 v[176:177], v[168:169], v[176:177], s[30:31] op_sel_hi:[1,1,0]
	v_pk_fma_f32 v[178:179], v[170:171], v[178:179], s[30:31] op_sel_hi:[1,1,0]
	v_pk_fma_f32 v[180:181], v[172:173], v[180:181], s[30:31] op_sel_hi:[1,1,0]
	v_pk_fma_f32 v[182:183], v[174:175], v[182:183], s[30:31] op_sel_hi:[1,1,0]
	v_pk_fma_f32 v[176:177], v[168:169], v[176:177], s[34:35] op_sel_hi:[1,1,0]
	v_pk_fma_f32 v[178:179], v[170:171], v[178:179], s[34:35] op_sel_hi:[1,1,0]
	v_pk_fma_f32 v[180:181], v[172:173], v[180:181], s[34:35] op_sel_hi:[1,1,0]
	v_pk_fma_f32 v[182:183], v[174:175], v[182:183], s[34:35] op_sel_hi:[1,1,0]
	v_pk_fma_f32 v[176:177], v[168:169], v[176:177], s[36:37] op_sel_hi:[1,1,0]
	v_pk_fma_f32 v[178:179], v[170:171], v[178:179], s[36:37] op_sel_hi:[1,1,0]
	v_pk_fma_f32 v[180:181], v[172:173], v[180:181], s[36:37] op_sel_hi:[1,1,0]
	v_pk_fma_f32 v[182:183], v[174:175], v[182:183], s[36:37] op_sel_hi:[1,1,0]
	v_pk_fma_f32 v[176:177], v[168:169], v[176:177], s[38:39] op_sel_hi:[1,1,0]
	v_pk_fma_f32 v[178:179], v[170:171], v[178:179], s[38:39] op_sel_hi:[1,1,0]
	v_pk_fma_f32 v[180:181], v[172:173], v[180:181], s[38:39] op_sel_hi:[1,1,0]
	v_pk_fma_f32 v[182:183], v[174:175], v[182:183], s[38:39] op_sel_hi:[1,1,0]
	v_pk_fma_f32 v[176:177], v[168:169], v[176:177], s[40:41] op_sel_hi:[1,1,0]
	v_pk_fma_f32 v[178:179], v[170:171], v[178:179], s[40:41] op_sel_hi:[1,1,0]
	v_pk_fma_f32 v[180:181], v[172:173], v[180:181], s[40:41] op_sel_hi:[1,1,0]
	v_pk_fma_f32 v[182:183], v[174:175], v[182:183], s[40:41] op_sel_hi:[1,1,0]
	v_pk_fma_f32 v[176:177], v[168:169], v[176:177], s[42:43] op_sel_hi:[1,1,0]
	v_pk_fma_f32 v[178:179], v[170:171], v[178:179], s[42:43] op_sel_hi:[1,1,0]
	v_pk_fma_f32 v[180:181], v[172:173], v[180:181], s[42:43] op_sel_hi:[1,1,0]
	v_pk_fma_f32 v[182:183], v[174:175], v[182:183], s[42:43] op_sel_hi:[1,1,0]
	v_pk_fma_f32 v[176:177], v[168:169], v[176:177], s[44:45] op_sel_hi:[1,1,0]
	v_pk_fma_f32 v[178:179], v[170:171], v[178:179], s[44:45] op_sel_hi:[1,1,0]
	v_pk_fma_f32 v[180:181], v[172:173], v[180:181], s[44:45] op_sel_hi:[1,1,0]
	v_pk_fma_f32 v[182:183], v[174:175], v[182:183], s[44:45] op_sel_hi:[1,1,0]
	v_pk_fma_f32 v[168:169], v[168:169], v[176:177], s[48:49] op_sel_hi:[1,1,0]
	v_pk_fma_f32 v[170:171], v[170:171], v[178:179], s[48:49] op_sel_hi:[1,1,0]
	v_pk_fma_f32 v[172:173], v[172:173], v[180:181], s[48:49] op_sel_hi:[1,1,0]
	v_pk_fma_f32 v[174:175], v[174:175], v[182:183], s[48:49] op_sel_hi:[1,1,0]
	v_pk_fma_f32 v[160:161], v[160:161], v[168:169], 0.5 op_sel_hi:[1,1,0]
	v_pk_fma_f32 v[162:163], v[162:163], v[170:171], 0.5 op_sel_hi:[1,1,0]
	v_pk_fma_f32 v[164:165], v[164:165], v[172:173], 0.5 op_sel_hi:[1,1,0]
	v_pk_fma_f32 v[166:167], v[166:167], v[174:175], 0.5 op_sel_hi:[1,1,0]
	v_pk_mul_f32 v[116:117], v[116:117], v[160:161]
	v_pk_mul_f32 v[118:119], v[118:119], v[162:163]
	v_pk_mul_f32 v[112:113], v[112:113], v[164:165]
	v_pk_mul_f32 v[114:115], v[114:115], v[166:167]
	v_cvt_pk_bf16_f32 v188, v116, v117
	v_cvt_pk_bf16_f32 v189, v118, v119
	v_cvt_pk_bf16_f32 v190, v112, v113
	v_cvt_pk_bf16_f32 v191, v114, v115
	global_store_dwordx4 v[196:197], v[188:191], off offset:256
	s_and_b64 vcc, exec, s[70:71]
	s_cbranch_vccz .Lg9_nostat_1
	v_pk_add_f32 v[160:161], v[124:125], v[126:127]
	v_pk_add_f32 v[162:163], v[120:121], v[122:123]
	v_pk_add_f32 v[164:165], v[116:117], v[118:119]
	v_pk_add_f32 v[166:167], v[112:113], v[114:115]
	v_pk_mul_f32 v[168:169], v[124:125], v[124:125]
	v_pk_mul_f32 v[170:171], v[116:117], v[116:117]
	v_pk_add_f32 v[160:161], v[160:161], v[162:163]
	v_pk_add_f32 v[164:165], v[164:165], v[166:167]
	v_pk_fma_f32 v[168:169], v[126:127], v[126:127], v[168:169]
	v_pk_fma_f32 v[170:171], v[118:119], v[118:119], v[170:171]
	v_pk_fma_f32 v[168:169], v[120:121], v[120:121], v[168:169]
	v_pk_fma_f32 v[170:171], v[112:113], v[112:113], v[170:171]
	v_pk_fma_f32 v[168:169], v[122:123], v[122:123], v[168:169]
	v_pk_fma_f32 v[170:171], v[114:115], v[114:115], v[170:171]
	v_pk_add_f32 v[160:161], v[160:161], v[164:165]
	v_pk_add_f32 v[168:169], v[168:169], v[170:171]
	s_nop 0
	v_add_f32_e32 v198, v160, v161
	v_add_f32_e32 v200, v168, v169
	v_mov_b32_e32 v199, v198
	s_nop 1
	v_permlane16_swap_b32 v199, v198
	s_nop 1
	v_add_f32_e32 v198, v199, v198
	v_mov_b32_e32 v202, v198
	v_mov_b32_e32 v201, v200
	s_nop 1
	v_permlane32_swap_b32 v202, v198
	s_nop 1
	s_nop 1
	v_permlane16_swap_b32 v201, v200
	s_nop 1
	v_add_f32_e32 v199, v201, v200
	v_mov_b32_e32 v203, v199
	s_nop 1
	v_permlane32_swap_b32 v203, v199
	s_nop 1
	s_and_saveexec_b64 s[4:5], s[6:7]
	v_lshlrev_b64 v[194:195], 8, v[192:193]
	v_lshl_add_u64 v[194:195], s[16:17], 0, v[194:195]
	v_lshl_add_u64 v[194:195], s[68:69], 3, v[194:195]
	v_pk_add_f32 v[200:201], v[202:203], v[198:199]
	global_store_dwordx2 v[194:195], v[200:201], off
	s_or_b64 exec, exec, s[4:5]
.Lg9_nostat_1:
	v_add_u32_e32 v192, 0x20, v148
	v_ashrrev_i32_e32 v193, 31, v192
	v_lshlrev_b64 v[194:195], 12, v[192:193]
	v_lshl_add_u64 v[196:197], v[146:147], 0, v[194:195]
	v_pk_add_f32 v[108:109], v[108:109], v[76:77]
	v_pk_add_f32 v[110:111], v[110:111], v[78:79]
	v_pk_add_f32 v[104:105], v[104:105], v[68:69]
	v_pk_add_f32 v[106:107], v[106:107], v[70:71]
	v_med3_f32 v160, v108, s78, v158
	v_med3_f32 v161, v109, s78, v158
	v_med3_f32 v162, v110, s78, v158
	v_med3_f32 v163, v111, s78, v158
	v_med3_f32 v164, v104, s78, v158
	v_med3_f32 v165, v105, s78, v158
	v_med3_f32 v166, v106, s78, v158
	v_med3_f32 v167, v107, s78, v158
	v_pk_mul_f32 v[168:169], v[160:161], v[160:161]
	v_pk_mul_f32 v[170:171], v[162:163], v[162:163]
	v_pk_mul_f32 v[172:173], v[164:165], v[164:165]
	v_pk_mul_f32 v[174:175], v[166:167], v[166:167]
	v_pk_fma_f32 v[168:169], v[168:169], s[20:21], -1.0 op_sel_hi:[1,0,0]
	v_pk_fma_f32 v[170:171], v[170:171], s[20:21], -1.0 op_sel_hi:[1,0,0]
	v_pk_fma_f32 v[172:173], v[172:173], s[20:21], -1.0 op_sel_hi:[1,0,0]
	v_pk_fma_f32 v[174:175], v[174:175], s[20:21], -1.0 op_sel_hi:[1,0,0]
	v_pk_fma_f32 v[176:177], v[168:169], s[22:23], v[150:151] op_sel_hi:[1,0,0] neg_lo:[1,0,0] neg_hi:[1,0,0]
	v_pk_fma_f32 v[178:179], v[170:171], s[22:23], v[150:151] op_sel_hi:[1,0,0] neg_lo:[1,0,0] neg_hi:[1,0,0]
	v_pk_fma_f32 v[180:181], v[172:173], s[22:23], v[150:151] op_sel_hi:[1,0,0] neg_lo:[1,0,0] neg_hi:[1,0,0]
	v_pk_fma_f32 v[182:183], v[174:175], s[22:23], v[150:151] op_sel_hi:[1,0,0] neg_lo:[1,0,0] neg_hi:[1,0,0]
	v_pk_fma_f32 v[176:177], v[168:169], v[176:177], s[26:27] op_sel_hi:[1,1,0]
	v_pk_fma_f32 v[178:179], v[170:171], v[178:179], s[26:27] op_sel_hi:[1,1,0]
	v_pk_fma_f32 v[180:181], v[172:173], v[180:181], s[26:27] op_sel_hi:[1,1,0]
	v_pk_fma_f32 v[182:183], v[174:175], v[182:183], s[26:27] op_sel_hi:[1,1,0]
	v_pk_fma_f32 v[176:177], v[168:169], v[176:177], s[28:29] op_sel_hi:[1,1,0]
	v_pk_fma_f32 v[178:179], v[170:171], v[178:179], s[28:29] op_sel_hi:[1,1,0]
	v_pk_fma_f32 v[180:181], v[172:173], v[180:181], s[28:29] op_sel_hi:[1,1,0]
	v_pk_fma_f32 v[182:183], v[174:175], v[182:183], s[28:29] op_sel_hi:[1,1,0]
	v_pk_fma_f32 v[176:177], v[168:169], v[176:177], s[30:31] op_sel_hi:[1,1,0]
	v_pk_fma_f32 v[178:179], v[170:171], v[178:179], s[30:31] op_sel_hi:[1,1,0]
	v_pk_fma_f32 v[180:181], v[172:173], v[180:181], s[30:31] op_sel_hi:[1,1,0]
	v_pk_fma_f32 v[182:183], v[174:175], v[182:183], s[30:31] op_sel_hi:[1,1,0]
	v_pk_fma_f32 v[176:177], v[168:169], v[176:177], s[34:35] op_sel_hi:[1,1,0]
	v_pk_fma_f32 v[178:179], v[170:171], v[178:179], s[34:35] op_sel_hi:[1,1,0]
	v_pk_fma_f32 v[180:181], v[172:173], v[180:181], s[34:35] op_sel_hi:[1,1,0]
	v_pk_fma_f32 v[182:183], v[174:175], v[182:183], s[34:35] op_sel_hi:[1,1,0]
	v_pk_fma_f32 v[176:177], v[168:169], v[176:177], s[36:37] op_sel_hi:[1,1,0]
	v_pk_fma_f32 v[178:179], v[170:171], v[178:179], s[36:37] op_sel_hi:[1,1,0]
	v_pk_fma_f32 v[180:181], v[172:173], v[180:181], s[36:37] op_sel_hi:[1,1,0]
	v_pk_fma_f32 v[182:183], v[174:175], v[182:183], s[36:37] op_sel_hi:[1,1,0]
	v_pk_fma_f32 v[176:177], v[168:169], v[176:177], s[38:39] op_sel_hi:[1,1,0]
	v_pk_fma_f32 v[178:179], v[170:171], v[178:179], s[38:39] op_sel_hi:[1,1,0]
	v_pk_fma_f32 v[180:181], v[172:173], v[180:181], s[38:39] op_sel_hi:[1,1,0]
	v_pk_fma_f32 v[182:183], v[174:175], v[182:183], s[38:39] op_sel_hi:[1,1,0]
	v_pk_fma_f32 v[176:177], v[168:169], v[176:177], s[40:41] op_sel_hi:[1,1,0]
	v_pk_fma_f32 v[178:179], v[170:171], v[178:179], s[40:41] op_sel_hi:[1,1,0]
	v_pk_fma_f32 v[180:181], v[172:173], v[180:181], s[40:41] op_sel_hi:[1,1,0]
	v_pk_fma_f32 v[182:183], v[174:175], v[182:183], s[40:41] op_sel_hi:[1,1,0]
	v_pk_fma_f32 v[176:177], v[168:169], v[176:177], s[42:43] op_sel_hi:[1,1,0]
	v_pk_fma_f32 v[178:179], v[170:171], v[178:179], s[42:43] op_sel_hi:[1,1,0]
	v_pk_fma_f32 v[180:181], v[172:173], v[180:181], s[42:43] op_sel_hi:[1,1,0]
	v_pk_fma_f32 v[182:183], v[174:175], v[182:183], s[42:43] op_sel_hi:[1,1,0]
	v_pk_fma_f32 v[176:177], v[168:169], v[176:177], s[44:45] op_sel_hi:[1,1,0]
	v_pk_fma_f32 v[178:179], v[170:171], v[178:179], s[44:45] op_sel_hi:[1,1,0]
	v_pk_fma_f32 v[180:181], v[172:173], v[180:181], s[44:45] op_sel_hi:[1,1,0]
	v_pk_fma_f32 v[182:183], v[174:175], v[182:183], s[44:45] op_sel_hi:[1,1,0]
	v_pk_fma_f32 v[168:169], v[168:169], v[176:177], s[48:49] op_sel_hi:[1,1,0]
	v_pk_fma_f32 v[170:171], v[170:171], v[178:179], s[48:49] op_sel_hi:[1,1,0]
	v_pk_fma_f32 v[172:173], v[172:173], v[180:181], s[48:49] op_sel_hi:[1,1,0]
	v_pk_fma_f32 v[174:175], v[174:175], v[182:183], s[48:49] op_sel_hi:[1,1,0]
	v_pk_fma_f32 v[160:161], v[160:161], v[168:169], 0.5 op_sel_hi:[1,1,0]
	v_pk_fma_f32 v[162:163], v[162:163], v[170:171], 0.5 op_sel_hi:[1,1,0]
	v_pk_fma_f32 v[164:165], v[164:165], v[172:173], 0.5 op_sel_hi:[1,1,0]
	v_pk_fma_f32 v[166:167], v[166:167], v[174:175], 0.5 op_sel_hi:[1,1,0]
	v_pk_mul_f32 v[108:109], v[108:109], v[160:161]
	v_pk_mul_f32 v[110:111], v[110:111], v[162:163]
	v_pk_mul_f32 v[104:105], v[104:105], v[164:165]
	v_pk_mul_f32 v[106:107], v[106:107], v[166:167]
	v_cvt_pk_bf16_f32 v184, v108, v109
	v_cvt_pk_bf16_f32 v185, v110, v111
	v_cvt_pk_bf16_f32 v186, v104, v105
	v_cvt_pk_bf16_f32 v187, v106, v107
	global_store_dwordx4 v[196:197], v[184:187], off
	v_pk_add_f32 v[100:101], v[100:101], v[60:61]
	v_pk_add_f32 v[102:103], v[102:103], v[62:63]
	v_pk_add_f32 v[96:97], v[96:97], v[56:57]
	v_pk_add_f32 v[98:99], v[98:99], v[58:59]
	v_med3_f32 v160, v100, s78, v158
	v_med3_f32 v161, v101, s78, v158
	v_med3_f32 v162, v102, s78, v158
	v_med3_f32 v163, v103, s78, v158
	v_med3_f32 v164, v96, s78, v158
	v_med3_f32 v165, v97, s78, v158
	v_med3_f32 v166, v98, s78, v158
	v_med3_f32 v167, v99, s78, v158
	v_pk_mul_f32 v[168:169], v[160:161], v[160:161]
	v_pk_mul_f32 v[170:171], v[162:163], v[162:163]
	v_pk_mul_f32 v[172:173], v[164:165], v[164:165]
	v_pk_mul_f32 v[174:175], v[166:167], v[166:167]
	v_pk_fma_f32 v[168:169], v[168:169], s[20:21], -1.0 op_sel_hi:[1,0,0]
	v_pk_fma_f32 v[170:171], v[170:171], s[20:21], -1.0 op_sel_hi:[1,0,0]
	v_pk_fma_f32 v[172:173], v[172:173], s[20:21], -1.0 op_sel_hi:[1,0,0]
	v_pk_fma_f32 v[174:175], v[174:175], s[20:21], -1.0 op_sel_hi:[1,0,0]
	v_pk_fma_f32 v[176:177], v[168:169], s[22:23], v[150:151] op_sel_hi:[1,0,0] neg_lo:[1,0,0] neg_hi:[1,0,0]
	v_pk_fma_f32 v[178:179], v[170:171], s[22:23], v[150:151] op_sel_hi:[1,0,0] neg_lo:[1,0,0] neg_hi:[1,0,0]
	v_pk_fma_f32 v[180:181], v[172:173], s[22:23], v[150:151] op_sel_hi:[1,0,0] neg_lo:[1,0,0] neg_hi:[1,0,0]
	v_pk_fma_f32 v[182:183], v[174:175], s[22:23], v[150:151] op_sel_hi:[1,0,0] neg_lo:[1,0,0] neg_hi:[1,0,0]
	v_pk_fma_f32 v[176:177], v[168:169], v[176:177], s[26:27] op_sel_hi:[1,1,0]
	v_pk_fma_f32 v[178:179], v[170:171], v[178:179], s[26:27] op_sel_hi:[1,1,0]
	v_pk_fma_f32 v[180:181], v[172:173], v[180:181], s[26:27] op_sel_hi:[1,1,0]
	v_pk_fma_f32 v[182:183], v[174:175], v[182:183], s[26:27] op_sel_hi:[1,1,0]
	v_pk_fma_f32 v[176:177], v[168:169], v[176:177], s[28:29] op_sel_hi:[1,1,0]
	v_pk_fma_f32 v[178:179], v[170:171], v[178:179], s[28:29] op_sel_hi:[1,1,0]
	v_pk_fma_f32 v[180:181], v[172:173], v[180:181], s[28:29] op_sel_hi:[1,1,0]
	v_pk_fma_f32 v[182:183], v[174:175], v[182:183], s[28:29] op_sel_hi:[1,1,0]
	v_pk_fma_f32 v[176:177], v[168:169], v[176:177], s[30:31] op_sel_hi:[1,1,0]
	v_pk_fma_f32 v[178:179], v[170:171], v[178:179], s[30:31] op_sel_hi:[1,1,0]
	v_pk_fma_f32 v[180:181], v[172:173], v[180:181], s[30:31] op_sel_hi:[1,1,0]
	v_pk_fma_f32 v[182:183], v[174:175], v[182:183], s[30:31] op_sel_hi:[1,1,0]
	v_pk_fma_f32 v[176:177], v[168:169], v[176:177], s[34:35] op_sel_hi:[1,1,0]
	v_pk_fma_f32 v[178:179], v[170:171], v[178:179], s[34:35] op_sel_hi:[1,1,0]
	v_pk_fma_f32 v[180:181], v[172:173], v[180:181], s[34:35] op_sel_hi:[1,1,0]
	v_pk_fma_f32 v[182:183], v[174:175], v[182:183], s[34:35] op_sel_hi:[1,1,0]
	v_pk_fma_f32 v[176:177], v[168:169], v[176:177], s[36:37] op_sel_hi:[1,1,0]
	v_pk_fma_f32 v[178:179], v[170:171], v[178:179], s[36:37] op_sel_hi:[1,1,0]
	v_pk_fma_f32 v[180:181], v[172:173], v[180:181], s[36:37] op_sel_hi:[1,1,0]
	v_pk_fma_f32 v[182:183], v[174:175], v[182:183], s[36:37] op_sel_hi:[1,1,0]
	v_pk_fma_f32 v[176:177], v[168:169], v[176:177], s[38:39] op_sel_hi:[1,1,0]
	v_pk_fma_f32 v[178:179], v[170:171], v[178:179], s[38:39] op_sel_hi:[1,1,0]
	v_pk_fma_f32 v[180:181], v[172:173], v[180:181], s[38:39] op_sel_hi:[1,1,0]
	v_pk_fma_f32 v[182:183], v[174:175], v[182:183], s[38:39] op_sel_hi:[1,1,0]
	v_pk_fma_f32 v[176:177], v[168:169], v[176:177], s[40:41] op_sel_hi:[1,1,0]
	v_pk_fma_f32 v[178:179], v[170:171], v[178:179], s[40:41] op_sel_hi:[1,1,0]
	v_pk_fma_f32 v[180:181], v[172:173], v[180:181], s[40:41] op_sel_hi:[1,1,0]
	v_pk_fma_f32 v[182:183], v[174:175], v[182:183], s[40:41] op_sel_hi:[1,1,0]
	v_pk_fma_f32 v[176:177], v[168:169], v[176:177], s[42:43] op_sel_hi:[1,1,0]
	v_pk_fma_f32 v[178:179], v[170:171], v[178:179], s[42:43] op_sel_hi:[1,1,0]
	v_pk_fma_f32 v[180:181], v[172:173], v[180:181], s[42:43] op_sel_hi:[1,1,0]
	v_pk_fma_f32 v[182:183], v[174:175], v[182:183], s[42:43] op_sel_hi:[1,1,0]
	v_pk_fma_f32 v[176:177], v[168:169], v[176:177], s[44:45] op_sel_hi:[1,1,0]
	v_pk_fma_f32 v[178:179], v[170:171], v[178:179], s[44:45] op_sel_hi:[1,1,0]
	v_pk_fma_f32 v[180:181], v[172:173], v[180:181], s[44:45] op_sel_hi:[1,1,0]
	v_pk_fma_f32 v[182:183], v[174:175], v[182:183], s[44:45] op_sel_hi:[1,1,0]
	v_pk_fma_f32 v[168:169], v[168:169], v[176:177], s[48:49] op_sel_hi:[1,1,0]
	v_pk_fma_f32 v[170:171], v[170:171], v[178:179], s[48:49] op_sel_hi:[1,1,0]
	v_pk_fma_f32 v[172:173], v[172:173], v[180:181], s[48:49] op_sel_hi:[1,1,0]
	v_pk_fma_f32 v[174:175], v[174:175], v[182:183], s[48:49] op_sel_hi:[1,1,0]
	v_pk_fma_f32 v[160:161], v[160:161], v[168:169], 0.5 op_sel_hi:[1,1,0]
	v_pk_fma_f32 v[162:163], v[162:163], v[170:171], 0.5 op_sel_hi:[1,1,0]
	v_pk_fma_f32 v[164:165], v[164:165], v[172:173], 0.5 op_sel_hi:[1,1,0]
	v_pk_fma_f32 v[166:167], v[166:167], v[174:175], 0.5 op_sel_hi:[1,1,0]
	v_pk_mul_f32 v[100:101], v[100:101], v[160:161]
	v_pk_mul_f32 v[102:103], v[102:103], v[162:163]
	v_pk_mul_f32 v[96:97], v[96:97], v[164:165]
	v_pk_mul_f32 v[98:99], v[98:99], v[166:167]
	v_cvt_pk_bf16_f32 v188, v100, v101
	v_cvt_pk_bf16_f32 v189, v102, v103
	v_cvt_pk_bf16_f32 v190, v96, v97
	v_cvt_pk_bf16_f32 v191, v98, v99
	global_store_dwordx4 v[196:197], v[188:191], off offset:256
	s_and_b64 vcc, exec, s[70:71]
	s_cbranch_vccz .Lg9_nostat_2
	v_pk_add_f32 v[160:161], v[108:109], v[110:111]
	v_pk_add_f32 v[162:163], v[104:105], v[106:107]
	v_pk_add_f32 v[164:165], v[100:101], v[102:103]
	v_pk_add_f32 v[166:167], v[96:97], v[98:99]
	v_pk_mul_f32 v[168:169], v[108:109], v[108:109]
	v_pk_mul_f32 v[170:171], v[100:101], v[100:101]
	v_pk_add_f32 v[160:161], v[160:161], v[162:163]
	v_pk_add_f32 v[164:165], v[164:165], v[166:167]
	v_pk_fma_f32 v[168:169], v[110:111], v[110:111], v[168:169]
	v_pk_fma_f32 v[170:171], v[102:103], v[102:103], v[170:171]
	v_pk_fma_f32 v[168:169], v[104:105], v[104:105], v[168:169]
	v_pk_fma_f32 v[170:171], v[96:97], v[96:97], v[170:171]
	v_pk_fma_f32 v[168:169], v[106:107], v[106:107], v[168:169]
	v_pk_fma_f32 v[170:171], v[98:99], v[98:99], v[170:171]
	v_pk_add_f32 v[160:161], v[160:161], v[164:165]
	v_pk_add_f32 v[168:169], v[168:169], v[170:171]
	s_nop 0
	v_add_f32_e32 v198, v160, v161
	v_add_f32_e32 v200, v168, v169
	v_mov_b32_e32 v199, v198
	s_nop 1
	v_permlane16_swap_b32 v199, v198
	s_nop 1
	v_add_f32_e32 v198, v199, v198
	v_mov_b32_e32 v202, v198
	v_mov_b32_e32 v201, v200
	s_nop 1
	v_permlane32_swap_b32 v202, v198
	s_nop 1
	s_nop 1
	v_permlane16_swap_b32 v201, v200
	s_nop 1
	v_add_f32_e32 v199, v201, v200
	v_mov_b32_e32 v203, v199
	s_nop 1
	v_permlane32_swap_b32 v203, v199
	s_nop 1
	s_and_saveexec_b64 s[4:5], s[6:7]
	v_lshlrev_b64 v[194:195], 8, v[192:193]
	v_lshl_add_u64 v[194:195], s[16:17], 0, v[194:195]
	v_lshl_add_u64 v[194:195], s[68:69], 3, v[194:195]
	v_pk_add_f32 v[200:201], v[202:203], v[198:199]
	global_store_dwordx2 v[194:195], v[200:201], off
	s_or_b64 exec, exec, s[4:5]
.Lg9_nostat_2:
	v_add_u32_e32 v192, 0x30, v148
	v_ashrrev_i32_e32 v193, 31, v192
	v_lshlrev_b64 v[194:195], 12, v[192:193]
	v_lshl_add_u64 v[196:197], v[146:147], 0, v[194:195]
	v_pk_add_f32 v[92:93], v[92:93], v[76:77]
	v_pk_add_f32 v[94:95], v[94:95], v[78:79]
	v_pk_add_f32 v[88:89], v[88:89], v[68:69]
	v_pk_add_f32 v[90:91], v[90:91], v[70:71]
	v_med3_f32 v160, v92, s78, v158
	v_med3_f32 v161, v93, s78, v158
	v_med3_f32 v162, v94, s78, v158
	v_med3_f32 v163, v95, s78, v158
	v_med3_f32 v164, v88, s78, v158
	v_med3_f32 v165, v89, s78, v158
	v_med3_f32 v166, v90, s78, v158
	v_med3_f32 v167, v91, s78, v158
	v_pk_mul_f32 v[168:169], v[160:161], v[160:161]
	v_pk_mul_f32 v[170:171], v[162:163], v[162:163]
	v_pk_mul_f32 v[172:173], v[164:165], v[164:165]
	v_pk_mul_f32 v[174:175], v[166:167], v[166:167]
	v_pk_fma_f32 v[168:169], v[168:169], s[20:21], -1.0 op_sel_hi:[1,0,0]
	v_pk_fma_f32 v[170:171], v[170:171], s[20:21], -1.0 op_sel_hi:[1,0,0]
	v_pk_fma_f32 v[172:173], v[172:173], s[20:21], -1.0 op_sel_hi:[1,0,0]
	v_pk_fma_f32 v[174:175], v[174:175], s[20:21], -1.0 op_sel_hi:[1,0,0]
	v_pk_fma_f32 v[176:177], v[168:169], s[22:23], v[150:151] op_sel_hi:[1,0,0] neg_lo:[1,0,0] neg_hi:[1,0,0]
	v_pk_fma_f32 v[178:179], v[170:171], s[22:23], v[150:151] op_sel_hi:[1,0,0] neg_lo:[1,0,0] neg_hi:[1,0,0]
	v_pk_fma_f32 v[180:181], v[172:173], s[22:23], v[150:151] op_sel_hi:[1,0,0] neg_lo:[1,0,0] neg_hi:[1,0,0]
	v_pk_fma_f32 v[182:183], v[174:175], s[22:23], v[150:151] op_sel_hi:[1,0,0] neg_lo:[1,0,0] neg_hi:[1,0,0]
	v_pk_fma_f32 v[176:177], v[168:169], v[176:177], s[26:27] op_sel_hi:[1,1,0]
	v_pk_fma_f32 v[178:179], v[170:171], v[178:179], s[26:27] op_sel_hi:[1,1,0]
	v_pk_fma_f32 v[180:181], v[172:173], v[180:181], s[26:27] op_sel_hi:[1,1,0]
	v_pk_fma_f32 v[182:183], v[174:175], v[182:183], s[26:27] op_sel_hi:[1,1,0]
	v_pk_fma_f32 v[176:177], v[168:169], v[176:177], s[28:29] op_sel_hi:[1,1,0]
	v_pk_fma_f32 v[178:179], v[170:171], v[178:179], s[28:29] op_sel_hi:[1,1,0]
	v_pk_fma_f32 v[180:181], v[172:173], v[180:181], s[28:29] op_sel_hi:[1,1,0]
	v_pk_fma_f32 v[182:183], v[174:175], v[182:183], s[28:29] op_sel_hi:[1,1,0]
	v_pk_fma_f32 v[176:177], v[168:169], v[176:177], s[30:31] op_sel_hi:[1,1,0]
	v_pk_fma_f32 v[178:179], v[170:171], v[178:179], s[30:31] op_sel_hi:[1,1,0]
	v_pk_fma_f32 v[180:181], v[172:173], v[180:181], s[30:31] op_sel_hi:[1,1,0]
	v_pk_fma_f32 v[182:183], v[174:175], v[182:183], s[30:31] op_sel_hi:[1,1,0]
	v_pk_fma_f32 v[176:177], v[168:169], v[176:177], s[34:35] op_sel_hi:[1,1,0]
	v_pk_fma_f32 v[178:179], v[170:171], v[178:179], s[34:35] op_sel_hi:[1,1,0]
	v_pk_fma_f32 v[180:181], v[172:173], v[180:181], s[34:35] op_sel_hi:[1,1,0]
	v_pk_fma_f32 v[182:183], v[174:175], v[182:183], s[34:35] op_sel_hi:[1,1,0]
	v_pk_fma_f32 v[176:177], v[168:169], v[176:177], s[36:37] op_sel_hi:[1,1,0]
	v_pk_fma_f32 v[178:179], v[170:171], v[178:179], s[36:37] op_sel_hi:[1,1,0]
	v_pk_fma_f32 v[180:181], v[172:173], v[180:181], s[36:37] op_sel_hi:[1,1,0]
	v_pk_fma_f32 v[182:183], v[174:175], v[182:183], s[36:37] op_sel_hi:[1,1,0]
	v_pk_fma_f32 v[176:177], v[168:169], v[176:177], s[38:39] op_sel_hi:[1,1,0]
	v_pk_fma_f32 v[178:179], v[170:171], v[178:179], s[38:39] op_sel_hi:[1,1,0]
	v_pk_fma_f32 v[180:181], v[172:173], v[180:181], s[38:39] op_sel_hi:[1,1,0]
	v_pk_fma_f32 v[182:183], v[174:175], v[182:183], s[38:39] op_sel_hi:[1,1,0]
	v_pk_fma_f32 v[176:177], v[168:169], v[176:177], s[40:41] op_sel_hi:[1,1,0]
	v_pk_fma_f32 v[178:179], v[170:171], v[178:179], s[40:41] op_sel_hi:[1,1,0]
	v_pk_fma_f32 v[180:181], v[172:173], v[180:181], s[40:41] op_sel_hi:[1,1,0]
	v_pk_fma_f32 v[182:183], v[174:175], v[182:183], s[40:41] op_sel_hi:[1,1,0]
	v_pk_fma_f32 v[176:177], v[168:169], v[176:177], s[42:43] op_sel_hi:[1,1,0]
	v_pk_fma_f32 v[178:179], v[170:171], v[178:179], s[42:43] op_sel_hi:[1,1,0]
	v_pk_fma_f32 v[180:181], v[172:173], v[180:181], s[42:43] op_sel_hi:[1,1,0]
	v_pk_fma_f32 v[182:183], v[174:175], v[182:183], s[42:43] op_sel_hi:[1,1,0]
	v_pk_fma_f32 v[176:177], v[168:169], v[176:177], s[44:45] op_sel_hi:[1,1,0]
	v_pk_fma_f32 v[178:179], v[170:171], v[178:179], s[44:45] op_sel_hi:[1,1,0]
	v_pk_fma_f32 v[180:181], v[172:173], v[180:181], s[44:45] op_sel_hi:[1,1,0]
	v_pk_fma_f32 v[182:183], v[174:175], v[182:183], s[44:45] op_sel_hi:[1,1,0]
	v_pk_fma_f32 v[168:169], v[168:169], v[176:177], s[48:49] op_sel_hi:[1,1,0]
	v_pk_fma_f32 v[170:171], v[170:171], v[178:179], s[48:49] op_sel_hi:[1,1,0]
	v_pk_fma_f32 v[172:173], v[172:173], v[180:181], s[48:49] op_sel_hi:[1,1,0]
	v_pk_fma_f32 v[174:175], v[174:175], v[182:183], s[48:49] op_sel_hi:[1,1,0]
	v_pk_fma_f32 v[160:161], v[160:161], v[168:169], 0.5 op_sel_hi:[1,1,0]
	v_pk_fma_f32 v[162:163], v[162:163], v[170:171], 0.5 op_sel_hi:[1,1,0]
	v_pk_fma_f32 v[164:165], v[164:165], v[172:173], 0.5 op_sel_hi:[1,1,0]
	v_pk_fma_f32 v[166:167], v[166:167], v[174:175], 0.5 op_sel_hi:[1,1,0]
	v_pk_mul_f32 v[92:93], v[92:93], v[160:161]
	v_pk_mul_f32 v[94:95], v[94:95], v[162:163]
	v_pk_mul_f32 v[88:89], v[88:89], v[164:165]
	v_pk_mul_f32 v[90:91], v[90:91], v[166:167]
	v_cvt_pk_bf16_f32 v184, v92, v93
	v_cvt_pk_bf16_f32 v185, v94, v95
	v_cvt_pk_bf16_f32 v186, v88, v89
	v_cvt_pk_bf16_f32 v187, v90, v91
	global_store_dwordx4 v[196:197], v[184:187], off
	v_pk_add_f32 v[84:85], v[84:85], v[60:61]
	v_pk_add_f32 v[86:87], v[86:87], v[62:63]
	v_pk_add_f32 v[80:81], v[80:81], v[56:57]
	v_pk_add_f32 v[82:83], v[82:83], v[58:59]
	v_med3_f32 v160, v84, s78, v158
	v_med3_f32 v161, v85, s78, v158
	v_med3_f32 v162, v86, s78, v158
	v_med3_f32 v163, v87, s78, v158
	v_med3_f32 v164, v80, s78, v158
	v_med3_f32 v165, v81, s78, v158
	v_med3_f32 v166, v82, s78, v158
	v_med3_f32 v167, v83, s78, v158
	v_pk_mul_f32 v[168:169], v[160:161], v[160:161]
	v_pk_mul_f32 v[170:171], v[162:163], v[162:163]
	v_pk_mul_f32 v[172:173], v[164:165], v[164:165]
	v_pk_mul_f32 v[174:175], v[166:167], v[166:167]
	v_pk_fma_f32 v[168:169], v[168:169], s[20:21], -1.0 op_sel_hi:[1,0,0]
	v_pk_fma_f32 v[170:171], v[170:171], s[20:21], -1.0 op_sel_hi:[1,0,0]
	v_pk_fma_f32 v[172:173], v[172:173], s[20:21], -1.0 op_sel_hi:[1,0,0]
	v_pk_fma_f32 v[174:175], v[174:175], s[20:21], -1.0 op_sel_hi:[1,0,0]
	v_pk_fma_f32 v[176:177], v[168:169], s[22:23], v[150:151] op_sel_hi:[1,0,0] neg_lo:[1,0,0] neg_hi:[1,0,0]
	v_pk_fma_f32 v[178:179], v[170:171], s[22:23], v[150:151] op_sel_hi:[1,0,0] neg_lo:[1,0,0] neg_hi:[1,0,0]
	v_pk_fma_f32 v[180:181], v[172:173], s[22:23], v[150:151] op_sel_hi:[1,0,0] neg_lo:[1,0,0] neg_hi:[1,0,0]
	v_pk_fma_f32 v[182:183], v[174:175], s[22:23], v[150:151] op_sel_hi:[1,0,0] neg_lo:[1,0,0] neg_hi:[1,0,0]
	v_pk_fma_f32 v[176:177], v[168:169], v[176:177], s[26:27] op_sel_hi:[1,1,0]
	v_pk_fma_f32 v[178:179], v[170:171], v[178:179], s[26:27] op_sel_hi:[1,1,0]
	v_pk_fma_f32 v[180:181], v[172:173], v[180:181], s[26:27] op_sel_hi:[1,1,0]
	v_pk_fma_f32 v[182:183], v[174:175], v[182:183], s[26:27] op_sel_hi:[1,1,0]
	v_pk_fma_f32 v[176:177], v[168:169], v[176:177], s[28:29] op_sel_hi:[1,1,0]
	v_pk_fma_f32 v[178:179], v[170:171], v[178:179], s[28:29] op_sel_hi:[1,1,0]
	v_pk_fma_f32 v[180:181], v[172:173], v[180:181], s[28:29] op_sel_hi:[1,1,0]
	v_pk_fma_f32 v[182:183], v[174:175], v[182:183], s[28:29] op_sel_hi:[1,1,0]
	v_pk_fma_f32 v[176:177], v[168:169], v[176:177], s[30:31] op_sel_hi:[1,1,0]
	v_pk_fma_f32 v[178:179], v[170:171], v[178:179], s[30:31] op_sel_hi:[1,1,0]
	v_pk_fma_f32 v[180:181], v[172:173], v[180:181], s[30:31] op_sel_hi:[1,1,0]
	v_pk_fma_f32 v[182:183], v[174:175], v[182:183], s[30:31] op_sel_hi:[1,1,0]
	v_pk_fma_f32 v[176:177], v[168:169], v[176:177], s[34:35] op_sel_hi:[1,1,0]
	v_pk_fma_f32 v[178:179], v[170:171], v[178:179], s[34:35] op_sel_hi:[1,1,0]
	v_pk_fma_f32 v[180:181], v[172:173], v[180:181], s[34:35] op_sel_hi:[1,1,0]
	v_pk_fma_f32 v[182:183], v[174:175], v[182:183], s[34:35] op_sel_hi:[1,1,0]
	v_pk_fma_f32 v[176:177], v[168:169], v[176:177], s[36:37] op_sel_hi:[1,1,0]
	v_pk_fma_f32 v[178:179], v[170:171], v[178:179], s[36:37] op_sel_hi:[1,1,0]
	v_pk_fma_f32 v[180:181], v[172:173], v[180:181], s[36:37] op_sel_hi:[1,1,0]
	v_pk_fma_f32 v[182:183], v[174:175], v[182:183], s[36:37] op_sel_hi:[1,1,0]
	v_pk_fma_f32 v[176:177], v[168:169], v[176:177], s[38:39] op_sel_hi:[1,1,0]
	v_pk_fma_f32 v[178:179], v[170:171], v[178:179], s[38:39] op_sel_hi:[1,1,0]
	v_pk_fma_f32 v[180:181], v[172:173], v[180:181], s[38:39] op_sel_hi:[1,1,0]
	v_pk_fma_f32 v[182:183], v[174:175], v[182:183], s[38:39] op_sel_hi:[1,1,0]
	v_pk_fma_f32 v[176:177], v[168:169], v[176:177], s[40:41] op_sel_hi:[1,1,0]
	v_pk_fma_f32 v[178:179], v[170:171], v[178:179], s[40:41] op_sel_hi:[1,1,0]
	v_pk_fma_f32 v[180:181], v[172:173], v[180:181], s[40:41] op_sel_hi:[1,1,0]
	v_pk_fma_f32 v[182:183], v[174:175], v[182:183], s[40:41] op_sel_hi:[1,1,0]
	v_pk_fma_f32 v[176:177], v[168:169], v[176:177], s[42:43] op_sel_hi:[1,1,0]
	v_pk_fma_f32 v[178:179], v[170:171], v[178:179], s[42:43] op_sel_hi:[1,1,0]
	v_pk_fma_f32 v[180:181], v[172:173], v[180:181], s[42:43] op_sel_hi:[1,1,0]
	v_pk_fma_f32 v[182:183], v[174:175], v[182:183], s[42:43] op_sel_hi:[1,1,0]
	v_pk_fma_f32 v[176:177], v[168:169], v[176:177], s[44:45] op_sel_hi:[1,1,0]
	v_pk_fma_f32 v[178:179], v[170:171], v[178:179], s[44:45] op_sel_hi:[1,1,0]
	v_pk_fma_f32 v[180:181], v[172:173], v[180:181], s[44:45] op_sel_hi:[1,1,0]
	v_pk_fma_f32 v[182:183], v[174:175], v[182:183], s[44:45] op_sel_hi:[1,1,0]
	v_pk_fma_f32 v[168:169], v[168:169], v[176:177], s[48:49] op_sel_hi:[1,1,0]
	v_pk_fma_f32 v[170:171], v[170:171], v[178:179], s[48:49] op_sel_hi:[1,1,0]
	v_pk_fma_f32 v[172:173], v[172:173], v[180:181], s[48:49] op_sel_hi:[1,1,0]
	v_pk_fma_f32 v[174:175], v[174:175], v[182:183], s[48:49] op_sel_hi:[1,1,0]
	v_pk_fma_f32 v[160:161], v[160:161], v[168:169], 0.5 op_sel_hi:[1,1,0]
	v_pk_fma_f32 v[162:163], v[162:163], v[170:171], 0.5 op_sel_hi:[1,1,0]
	v_pk_fma_f32 v[164:165], v[164:165], v[172:173], 0.5 op_sel_hi:[1,1,0]
	v_pk_fma_f32 v[166:167], v[166:167], v[174:175], 0.5 op_sel_hi:[1,1,0]
	v_pk_mul_f32 v[84:85], v[84:85], v[160:161]
	v_pk_mul_f32 v[86:87], v[86:87], v[162:163]
	v_pk_mul_f32 v[80:81], v[80:81], v[164:165]
	v_pk_mul_f32 v[82:83], v[82:83], v[166:167]
	v_cvt_pk_bf16_f32 v188, v84, v85
	v_cvt_pk_bf16_f32 v189, v86, v87
	v_cvt_pk_bf16_f32 v190, v80, v81
	v_cvt_pk_bf16_f32 v191, v82, v83
	global_store_dwordx4 v[196:197], v[188:191], off offset:256
	s_and_b64 vcc, exec, s[70:71]
	s_cbranch_vccz .Lg9_nostat_3
	v_pk_add_f32 v[160:161], v[92:93], v[94:95]
	v_pk_add_f32 v[162:163], v[88:89], v[90:91]
	v_pk_add_f32 v[164:165], v[84:85], v[86:87]
	v_pk_add_f32 v[166:167], v[80:81], v[82:83]
	v_pk_mul_f32 v[168:169], v[92:93], v[92:93]
	v_pk_mul_f32 v[170:171], v[84:85], v[84:85]
	v_pk_add_f32 v[160:161], v[160:161], v[162:163]
	v_pk_add_f32 v[164:165], v[164:165], v[166:167]
	v_pk_fma_f32 v[168:169], v[94:95], v[94:95], v[168:169]
	v_pk_fma_f32 v[170:171], v[86:87], v[86:87], v[170:171]
	v_pk_fma_f32 v[168:169], v[88:89], v[88:89], v[168:169]
	v_pk_fma_f32 v[170:171], v[80:81], v[80:81], v[170:171]
	v_pk_fma_f32 v[168:169], v[90:91], v[90:91], v[168:169]
	v_pk_fma_f32 v[170:171], v[82:83], v[82:83], v[170:171]
	v_pk_add_f32 v[160:161], v[160:161], v[164:165]
	v_pk_add_f32 v[168:169], v[168:169], v[170:171]
	s_nop 0
	v_add_f32_e32 v198, v160, v161
	v_add_f32_e32 v200, v168, v169
	v_mov_b32_e32 v199, v198
	s_nop 1
	v_permlane16_swap_b32 v199, v198
	s_nop 1
	v_add_f32_e32 v198, v199, v198
	v_mov_b32_e32 v202, v198
	v_mov_b32_e32 v201, v200
	s_nop 1
	v_permlane32_swap_b32 v202, v198
	s_nop 1
	s_nop 1
	v_permlane16_swap_b32 v201, v200
	s_nop 1
	v_add_f32_e32 v199, v201, v200
	v_mov_b32_e32 v203, v199
	s_nop 1
	v_permlane32_swap_b32 v203, v199
	s_nop 1
	s_and_saveexec_b64 s[4:5], s[6:7]
	v_lshlrev_b64 v[194:195], 8, v[192:193]
	v_lshl_add_u64 v[194:195], s[16:17], 0, v[194:195]
	v_lshl_add_u64 v[194:195], s[68:69], 3, v[194:195]
	v_pk_add_f32 v[200:201], v[202:203], v[198:199]
	global_store_dwordx2 v[194:195], v[200:201], off
	s_or_b64 exec, exec, s[4:5]
.Lg9_nostat_3:
	v_add_u32_e32 v192, 0x80, v148
	v_ashrrev_i32_e32 v193, 31, v192
	v_lshlrev_b64 v[194:195], 12, v[192:193]
	v_lshl_add_u64 v[196:197], v[146:147], 0, v[194:195]
	v_pk_add_f32 v[72:73], v[72:73], v[76:77]
	v_pk_add_f32 v[74:75], v[74:75], v[78:79]
	v_pk_add_f32 v[64:65], v[64:65], v[68:69]
	v_pk_add_f32 v[66:67], v[66:67], v[70:71]
	v_med3_f32 v160, v72, s78, v158
	v_med3_f32 v161, v73, s78, v158
	v_med3_f32 v162, v74, s78, v158
	v_med3_f32 v163, v75, s78, v158
	v_med3_f32 v164, v64, s78, v158
	v_med3_f32 v165, v65, s78, v158
	v_med3_f32 v166, v66, s78, v158
	v_med3_f32 v167, v67, s78, v158
	v_pk_mul_f32 v[168:169], v[160:161], v[160:161]
	v_pk_mul_f32 v[170:171], v[162:163], v[162:163]
	v_pk_mul_f32 v[172:173], v[164:165], v[164:165]
	v_pk_mul_f32 v[174:175], v[166:167], v[166:167]
	v_pk_fma_f32 v[168:169], v[168:169], s[20:21], -1.0 op_sel_hi:[1,0,0]
	v_pk_fma_f32 v[170:171], v[170:171], s[20:21], -1.0 op_sel_hi:[1,0,0]
	v_pk_fma_f32 v[172:173], v[172:173], s[20:21], -1.0 op_sel_hi:[1,0,0]
	v_pk_fma_f32 v[174:175], v[174:175], s[20:21], -1.0 op_sel_hi:[1,0,0]
	v_pk_fma_f32 v[176:177], v[168:169], s[22:23], v[150:151] op_sel_hi:[1,0,0] neg_lo:[1,0,0] neg_hi:[1,0,0]
	v_pk_fma_f32 v[178:179], v[170:171], s[22:23], v[150:151] op_sel_hi:[1,0,0] neg_lo:[1,0,0] neg_hi:[1,0,0]
	v_pk_fma_f32 v[180:181], v[172:173], s[22:23], v[150:151] op_sel_hi:[1,0,0] neg_lo:[1,0,0] neg_hi:[1,0,0]
	v_pk_fma_f32 v[182:183], v[174:175], s[22:23], v[150:151] op_sel_hi:[1,0,0] neg_lo:[1,0,0] neg_hi:[1,0,0]
	v_pk_fma_f32 v[176:177], v[168:169], v[176:177], s[26:27] op_sel_hi:[1,1,0]
	v_pk_fma_f32 v[178:179], v[170:171], v[178:179], s[26:27] op_sel_hi:[1,1,0]
	v_pk_fma_f32 v[180:181], v[172:173], v[180:181], s[26:27] op_sel_hi:[1,1,0]
	v_pk_fma_f32 v[182:183], v[174:175], v[182:183], s[26:27] op_sel_hi:[1,1,0]
	v_pk_fma_f32 v[176:177], v[168:169], v[176:177], s[28:29] op_sel_hi:[1,1,0]
	v_pk_fma_f32 v[178:179], v[170:171], v[178:179], s[28:29] op_sel_hi:[1,1,0]
	v_pk_fma_f32 v[180:181], v[172:173], v[180:181], s[28:29] op_sel_hi:[1,1,0]
	v_pk_fma_f32 v[182:183], v[174:175], v[182:183], s[28:29] op_sel_hi:[1,1,0]
	v_pk_fma_f32 v[176:177], v[168:169], v[176:177], s[30:31] op_sel_hi:[1,1,0]
	v_pk_fma_f32 v[178:179], v[170:171], v[178:179], s[30:31] op_sel_hi:[1,1,0]
	v_pk_fma_f32 v[180:181], v[172:173], v[180:181], s[30:31] op_sel_hi:[1,1,0]
	v_pk_fma_f32 v[182:183], v[174:175], v[182:183], s[30:31] op_sel_hi:[1,1,0]
	v_pk_fma_f32 v[176:177], v[168:169], v[176:177], s[34:35] op_sel_hi:[1,1,0]
	v_pk_fma_f32 v[178:179], v[170:171], v[178:179], s[34:35] op_sel_hi:[1,1,0]
	v_pk_fma_f32 v[180:181], v[172:173], v[180:181], s[34:35] op_sel_hi:[1,1,0]
	v_pk_fma_f32 v[182:183], v[174:175], v[182:183], s[34:35] op_sel_hi:[1,1,0]
	v_pk_fma_f32 v[176:177], v[168:169], v[176:177], s[36:37] op_sel_hi:[1,1,0]
	v_pk_fma_f32 v[178:179], v[170:171], v[178:179], s[36:37] op_sel_hi:[1,1,0]
	v_pk_fma_f32 v[180:181], v[172:173], v[180:181], s[36:37] op_sel_hi:[1,1,0]
	v_pk_fma_f32 v[182:183], v[174:175], v[182:183], s[36:37] op_sel_hi:[1,1,0]
	v_pk_fma_f32 v[176:177], v[168:169], v[176:177], s[38:39] op_sel_hi:[1,1,0]
	v_pk_fma_f32 v[178:179], v[170:171], v[178:179], s[38:39] op_sel_hi:[1,1,0]
	v_pk_fma_f32 v[180:181], v[172:173], v[180:181], s[38:39] op_sel_hi:[1,1,0]
	v_pk_fma_f32 v[182:183], v[174:175], v[182:183], s[38:39] op_sel_hi:[1,1,0]
	v_pk_fma_f32 v[176:177], v[168:169], v[176:177], s[40:41] op_sel_hi:[1,1,0]
	v_pk_fma_f32 v[178:179], v[170:171], v[178:179], s[40:41] op_sel_hi:[1,1,0]
	v_pk_fma_f32 v[180:181], v[172:173], v[180:181], s[40:41] op_sel_hi:[1,1,0]
	v_pk_fma_f32 v[182:183], v[174:175], v[182:183], s[40:41] op_sel_hi:[1,1,0]
	v_pk_fma_f32 v[176:177], v[168:169], v[176:177], s[42:43] op_sel_hi:[1,1,0]
	v_pk_fma_f32 v[178:179], v[170:171], v[178:179], s[42:43] op_sel_hi:[1,1,0]
	v_pk_fma_f32 v[180:181], v[172:173], v[180:181], s[42:43] op_sel_hi:[1,1,0]
	v_pk_fma_f32 v[182:183], v[174:175], v[182:183], s[42:43] op_sel_hi:[1,1,0]
	v_pk_fma_f32 v[176:177], v[168:169], v[176:177], s[44:45] op_sel_hi:[1,1,0]
	v_pk_fma_f32 v[178:179], v[170:171], v[178:179], s[44:45] op_sel_hi:[1,1,0]
	v_pk_fma_f32 v[180:181], v[172:173], v[180:181], s[44:45] op_sel_hi:[1,1,0]
	v_pk_fma_f32 v[182:183], v[174:175], v[182:183], s[44:45] op_sel_hi:[1,1,0]
	v_pk_fma_f32 v[168:169], v[168:169], v[176:177], s[48:49] op_sel_hi:[1,1,0]
	v_pk_fma_f32 v[170:171], v[170:171], v[178:179], s[48:49] op_sel_hi:[1,1,0]
	v_pk_fma_f32 v[172:173], v[172:173], v[180:181], s[48:49] op_sel_hi:[1,1,0]
	v_pk_fma_f32 v[174:175], v[174:175], v[182:183], s[48:49] op_sel_hi:[1,1,0]
	v_pk_fma_f32 v[160:161], v[160:161], v[168:169], 0.5 op_sel_hi:[1,1,0]
	v_pk_fma_f32 v[162:163], v[162:163], v[170:171], 0.5 op_sel_hi:[1,1,0]
	v_pk_fma_f32 v[164:165], v[164:165], v[172:173], 0.5 op_sel_hi:[1,1,0]
	v_pk_fma_f32 v[166:167], v[166:167], v[174:175], 0.5 op_sel_hi:[1,1,0]
	v_pk_mul_f32 v[72:73], v[72:73], v[160:161]
	v_pk_mul_f32 v[74:75], v[74:75], v[162:163]
	v_pk_mul_f32 v[64:65], v[64:65], v[164:165]
	v_pk_mul_f32 v[66:67], v[66:67], v[166:167]
	v_cvt_pk_bf16_f32 v184, v72, v73
	v_cvt_pk_bf16_f32 v185, v74, v75
	v_cvt_pk_bf16_f32 v186, v64, v65
	v_cvt_pk_bf16_f32 v187, v66, v67
	global_store_dwordx4 v[196:197], v[184:187], off
	v_pk_add_f32 v[52:53], v[52:53], v[60:61]
	v_pk_add_f32 v[54:55], v[54:55], v[62:63]
	v_pk_add_f32 v[48:49], v[48:49], v[56:57]
	v_pk_add_f32 v[50:51], v[50:51], v[58:59]
	v_med3_f32 v160, v52, s78, v158
	v_med3_f32 v161, v53, s78, v158
	v_med3_f32 v162, v54, s78, v158
	v_med3_f32 v163, v55, s78, v158
	v_med3_f32 v164, v48, s78, v158
	v_med3_f32 v165, v49, s78, v158
	v_med3_f32 v166, v50, s78, v158
	v_med3_f32 v167, v51, s78, v158
	v_pk_mul_f32 v[168:169], v[160:161], v[160:161]
	v_pk_mul_f32 v[170:171], v[162:163], v[162:163]
	v_pk_mul_f32 v[172:173], v[164:165], v[164:165]
	v_pk_mul_f32 v[174:175], v[166:167], v[166:167]
	v_pk_fma_f32 v[168:169], v[168:169], s[20:21], -1.0 op_sel_hi:[1,0,0]
	v_pk_fma_f32 v[170:171], v[170:171], s[20:21], -1.0 op_sel_hi:[1,0,0]
	v_pk_fma_f32 v[172:173], v[172:173], s[20:21], -1.0 op_sel_hi:[1,0,0]
	v_pk_fma_f32 v[174:175], v[174:175], s[20:21], -1.0 op_sel_hi:[1,0,0]
	v_pk_fma_f32 v[176:177], v[168:169], s[22:23], v[150:151] op_sel_hi:[1,0,0] neg_lo:[1,0,0] neg_hi:[1,0,0]
	v_pk_fma_f32 v[178:179], v[170:171], s[22:23], v[150:151] op_sel_hi:[1,0,0] neg_lo:[1,0,0] neg_hi:[1,0,0]
	v_pk_fma_f32 v[180:181], v[172:173], s[22:23], v[150:151] op_sel_hi:[1,0,0] neg_lo:[1,0,0] neg_hi:[1,0,0]
	v_pk_fma_f32 v[182:183], v[174:175], s[22:23], v[150:151] op_sel_hi:[1,0,0] neg_lo:[1,0,0] neg_hi:[1,0,0]
	v_pk_fma_f32 v[176:177], v[168:169], v[176:177], s[26:27] op_sel_hi:[1,1,0]
	v_pk_fma_f32 v[178:179], v[170:171], v[178:179], s[26:27] op_sel_hi:[1,1,0]
	v_pk_fma_f32 v[180:181], v[172:173], v[180:181], s[26:27] op_sel_hi:[1,1,0]
	v_pk_fma_f32 v[182:183], v[174:175], v[182:183], s[26:27] op_sel_hi:[1,1,0]
	v_pk_fma_f32 v[176:177], v[168:169], v[176:177], s[28:29] op_sel_hi:[1,1,0]
	v_pk_fma_f32 v[178:179], v[170:171], v[178:179], s[28:29] op_sel_hi:[1,1,0]
	v_pk_fma_f32 v[180:181], v[172:173], v[180:181], s[28:29] op_sel_hi:[1,1,0]
	v_pk_fma_f32 v[182:183], v[174:175], v[182:183], s[28:29] op_sel_hi:[1,1,0]
	v_pk_fma_f32 v[176:177], v[168:169], v[176:177], s[30:31] op_sel_hi:[1,1,0]
	v_pk_fma_f32 v[178:179], v[170:171], v[178:179], s[30:31] op_sel_hi:[1,1,0]
	v_pk_fma_f32 v[180:181], v[172:173], v[180:181], s[30:31] op_sel_hi:[1,1,0]
	v_pk_fma_f32 v[182:183], v[174:175], v[182:183], s[30:31] op_sel_hi:[1,1,0]
	v_pk_fma_f32 v[176:177], v[168:169], v[176:177], s[34:35] op_sel_hi:[1,1,0]
	v_pk_fma_f32 v[178:179], v[170:171], v[178:179], s[34:35] op_sel_hi:[1,1,0]
	v_pk_fma_f32 v[180:181], v[172:173], v[180:181], s[34:35] op_sel_hi:[1,1,0]
	v_pk_fma_f32 v[182:183], v[174:175], v[182:183], s[34:35] op_sel_hi:[1,1,0]
	v_pk_fma_f32 v[176:177], v[168:169], v[176:177], s[36:37] op_sel_hi:[1,1,0]
	v_pk_fma_f32 v[178:179], v[170:171], v[178:179], s[36:37] op_sel_hi:[1,1,0]
	v_pk_fma_f32 v[180:181], v[172:173], v[180:181], s[36:37] op_sel_hi:[1,1,0]
	v_pk_fma_f32 v[182:183], v[174:175], v[182:183], s[36:37] op_sel_hi:[1,1,0]
	v_pk_fma_f32 v[176:177], v[168:169], v[176:177], s[38:39] op_sel_hi:[1,1,0]
	v_pk_fma_f32 v[178:179], v[170:171], v[178:179], s[38:39] op_sel_hi:[1,1,0]
	v_pk_fma_f32 v[180:181], v[172:173], v[180:181], s[38:39] op_sel_hi:[1,1,0]
	v_pk_fma_f32 v[182:183], v[174:175], v[182:183], s[38:39] op_sel_hi:[1,1,0]
	v_pk_fma_f32 v[176:177], v[168:169], v[176:177], s[40:41] op_sel_hi:[1,1,0]
	v_pk_fma_f32 v[178:179], v[170:171], v[178:179], s[40:41] op_sel_hi:[1,1,0]
	v_pk_fma_f32 v[180:181], v[172:173], v[180:181], s[40:41] op_sel_hi:[1,1,0]
	v_pk_fma_f32 v[182:183], v[174:175], v[182:183], s[40:41] op_sel_hi:[1,1,0]
	v_pk_fma_f32 v[176:177], v[168:169], v[176:177], s[42:43] op_sel_hi:[1,1,0]
	v_pk_fma_f32 v[178:179], v[170:171], v[178:179], s[42:43] op_sel_hi:[1,1,0]
	v_pk_fma_f32 v[180:181], v[172:173], v[180:181], s[42:43] op_sel_hi:[1,1,0]
	v_pk_fma_f32 v[182:183], v[174:175], v[182:183], s[42:43] op_sel_hi:[1,1,0]
	v_pk_fma_f32 v[176:177], v[168:169], v[176:177], s[44:45] op_sel_hi:[1,1,0]
	v_pk_fma_f32 v[178:179], v[170:171], v[178:179], s[44:45] op_sel_hi:[1,1,0]
	v_pk_fma_f32 v[180:181], v[172:173], v[180:181], s[44:45] op_sel_hi:[1,1,0]
	v_pk_fma_f32 v[182:183], v[174:175], v[182:183], s[44:45] op_sel_hi:[1,1,0]
	v_pk_fma_f32 v[168:169], v[168:169], v[176:177], s[48:49] op_sel_hi:[1,1,0]
	v_pk_fma_f32 v[170:171], v[170:171], v[178:179], s[48:49] op_sel_hi:[1,1,0]
	v_pk_fma_f32 v[172:173], v[172:173], v[180:181], s[48:49] op_sel_hi:[1,1,0]
	v_pk_fma_f32 v[174:175], v[174:175], v[182:183], s[48:49] op_sel_hi:[1,1,0]
	v_pk_fma_f32 v[160:161], v[160:161], v[168:169], 0.5 op_sel_hi:[1,1,0]
	v_pk_fma_f32 v[162:163], v[162:163], v[170:171], 0.5 op_sel_hi:[1,1,0]
	v_pk_fma_f32 v[164:165], v[164:165], v[172:173], 0.5 op_sel_hi:[1,1,0]
	v_pk_fma_f32 v[166:167], v[166:167], v[174:175], 0.5 op_sel_hi:[1,1,0]
	v_pk_mul_f32 v[52:53], v[52:53], v[160:161]
	v_pk_mul_f32 v[54:55], v[54:55], v[162:163]
	v_pk_mul_f32 v[48:49], v[48:49], v[164:165]
	v_pk_mul_f32 v[50:51], v[50:51], v[166:167]
	v_cvt_pk_bf16_f32 v188, v52, v53
	v_cvt_pk_bf16_f32 v189, v54, v55
	v_cvt_pk_bf16_f32 v190, v48, v49
	v_cvt_pk_bf16_f32 v191, v50, v51
	global_store_dwordx4 v[196:197], v[188:191], off offset:256
	s_and_b64 vcc, exec, s[70:71]
	s_cbranch_vccz .Lg9_nostat_4
	v_pk_add_f32 v[160:161], v[72:73], v[74:75]
	v_pk_add_f32 v[162:163], v[64:65], v[66:67]
	v_pk_add_f32 v[164:165], v[52:53], v[54:55]
	v_pk_add_f32 v[166:167], v[48:49], v[50:51]
	v_pk_mul_f32 v[168:169], v[72:73], v[72:73]
	v_pk_mul_f32 v[170:171], v[52:53], v[52:53]
	v_pk_add_f32 v[160:161], v[160:161], v[162:163]
	v_pk_add_f32 v[164:165], v[164:165], v[166:167]
	v_pk_fma_f32 v[168:169], v[74:75], v[74:75], v[168:169]
	v_pk_fma_f32 v[170:171], v[54:55], v[54:55], v[170:171]
	v_pk_fma_f32 v[168:169], v[64:65], v[64:65], v[168:169]
	v_pk_fma_f32 v[170:171], v[48:49], v[48:49], v[170:171]
	v_pk_fma_f32 v[168:169], v[66:67], v[66:67], v[168:169]
	v_pk_fma_f32 v[170:171], v[50:51], v[50:51], v[170:171]
	v_pk_add_f32 v[160:161], v[160:161], v[164:165]
	v_pk_add_f32 v[168:169], v[168:169], v[170:171]
	s_nop 0
	v_add_f32_e32 v198, v160, v161
	v_add_f32_e32 v200, v168, v169
	v_mov_b32_e32 v199, v198
	s_nop 1
	v_permlane16_swap_b32 v199, v198
	s_nop 1
	v_add_f32_e32 v198, v199, v198
	v_mov_b32_e32 v202, v198
	v_mov_b32_e32 v201, v200
	s_nop 1
	v_permlane32_swap_b32 v202, v198
	s_nop 1
	s_nop 1
	v_permlane16_swap_b32 v201, v200
	s_nop 1
	v_add_f32_e32 v199, v201, v200
	v_mov_b32_e32 v203, v199
	s_nop 1
	v_permlane32_swap_b32 v203, v199
	s_nop 1
	s_and_saveexec_b64 s[4:5], s[6:7]
	v_lshlrev_b64 v[194:195], 8, v[192:193]
	v_lshl_add_u64 v[194:195], s[16:17], 0, v[194:195]
	v_lshl_add_u64 v[194:195], s[68:69], 3, v[194:195]
	v_pk_add_f32 v[200:201], v[202:203], v[198:199]
	global_store_dwordx2 v[194:195], v[200:201], off
	s_or_b64 exec, exec, s[4:5]
.Lg9_nostat_4:
	v_add_u32_e32 v192, 0x90, v148
	v_ashrrev_i32_e32 v193, 31, v192
	v_lshlrev_b64 v[194:195], 12, v[192:193]
	v_lshl_add_u64 v[196:197], v[146:147], 0, v[194:195]
	v_pk_add_f32 v[44:45], v[44:45], v[76:77]
	v_pk_add_f32 v[46:47], v[46:47], v[78:79]
	v_pk_add_f32 v[40:41], v[40:41], v[68:69]
	v_pk_add_f32 v[42:43], v[42:43], v[70:71]
	v_med3_f32 v160, v44, s78, v158
	v_med3_f32 v161, v45, s78, v158
	v_med3_f32 v162, v46, s78, v158
	v_med3_f32 v163, v47, s78, v158
	v_med3_f32 v164, v40, s78, v158
	v_med3_f32 v165, v41, s78, v158
	v_med3_f32 v166, v42, s78, v158
	v_med3_f32 v167, v43, s78, v158
	v_pk_mul_f32 v[168:169], v[160:161], v[160:161]
	v_pk_mul_f32 v[170:171], v[162:163], v[162:163]
	v_pk_mul_f32 v[172:173], v[164:165], v[164:165]
	v_pk_mul_f32 v[174:175], v[166:167], v[166:167]
	v_pk_fma_f32 v[168:169], v[168:169], s[20:21], -1.0 op_sel_hi:[1,0,0]
	v_pk_fma_f32 v[170:171], v[170:171], s[20:21], -1.0 op_sel_hi:[1,0,0]
	v_pk_fma_f32 v[172:173], v[172:173], s[20:21], -1.0 op_sel_hi:[1,0,0]
	v_pk_fma_f32 v[174:175], v[174:175], s[20:21], -1.0 op_sel_hi:[1,0,0]
	v_pk_fma_f32 v[176:177], v[168:169], s[22:23], v[150:151] op_sel_hi:[1,0,0] neg_lo:[1,0,0] neg_hi:[1,0,0]
	v_pk_fma_f32 v[178:179], v[170:171], s[22:23], v[150:151] op_sel_hi:[1,0,0] neg_lo:[1,0,0] neg_hi:[1,0,0]
	v_pk_fma_f32 v[180:181], v[172:173], s[22:23], v[150:151] op_sel_hi:[1,0,0] neg_lo:[1,0,0] neg_hi:[1,0,0]
	v_pk_fma_f32 v[182:183], v[174:175], s[22:23], v[150:151] op_sel_hi:[1,0,0] neg_lo:[1,0,0] neg_hi:[1,0,0]
	v_pk_fma_f32 v[176:177], v[168:169], v[176:177], s[26:27] op_sel_hi:[1,1,0]
	v_pk_fma_f32 v[178:179], v[170:171], v[178:179], s[26:27] op_sel_hi:[1,1,0]
	v_pk_fma_f32 v[180:181], v[172:173], v[180:181], s[26:27] op_sel_hi:[1,1,0]
	v_pk_fma_f32 v[182:183], v[174:175], v[182:183], s[26:27] op_sel_hi:[1,1,0]
	v_pk_fma_f32 v[176:177], v[168:169], v[176:177], s[28:29] op_sel_hi:[1,1,0]
	v_pk_fma_f32 v[178:179], v[170:171], v[178:179], s[28:29] op_sel_hi:[1,1,0]
	v_pk_fma_f32 v[180:181], v[172:173], v[180:181], s[28:29] op_sel_hi:[1,1,0]
	v_pk_fma_f32 v[182:183], v[174:175], v[182:183], s[28:29] op_sel_hi:[1,1,0]
	v_pk_fma_f32 v[176:177], v[168:169], v[176:177], s[30:31] op_sel_hi:[1,1,0]
	v_pk_fma_f32 v[178:179], v[170:171], v[178:179], s[30:31] op_sel_hi:[1,1,0]
	v_pk_fma_f32 v[180:181], v[172:173], v[180:181], s[30:31] op_sel_hi:[1,1,0]
	v_pk_fma_f32 v[182:183], v[174:175], v[182:183], s[30:31] op_sel_hi:[1,1,0]
	v_pk_fma_f32 v[176:177], v[168:169], v[176:177], s[34:35] op_sel_hi:[1,1,0]
	v_pk_fma_f32 v[178:179], v[170:171], v[178:179], s[34:35] op_sel_hi:[1,1,0]
	v_pk_fma_f32 v[180:181], v[172:173], v[180:181], s[34:35] op_sel_hi:[1,1,0]
	v_pk_fma_f32 v[182:183], v[174:175], v[182:183], s[34:35] op_sel_hi:[1,1,0]
	v_pk_fma_f32 v[176:177], v[168:169], v[176:177], s[36:37] op_sel_hi:[1,1,0]
	v_pk_fma_f32 v[178:179], v[170:171], v[178:179], s[36:37] op_sel_hi:[1,1,0]
	v_pk_fma_f32 v[180:181], v[172:173], v[180:181], s[36:37] op_sel_hi:[1,1,0]
	v_pk_fma_f32 v[182:183], v[174:175], v[182:183], s[36:37] op_sel_hi:[1,1,0]
	v_pk_fma_f32 v[176:177], v[168:169], v[176:177], s[38:39] op_sel_hi:[1,1,0]
	v_pk_fma_f32 v[178:179], v[170:171], v[178:179], s[38:39] op_sel_hi:[1,1,0]
	v_pk_fma_f32 v[180:181], v[172:173], v[180:181], s[38:39] op_sel_hi:[1,1,0]
	v_pk_fma_f32 v[182:183], v[174:175], v[182:183], s[38:39] op_sel_hi:[1,1,0]
	v_pk_fma_f32 v[176:177], v[168:169], v[176:177], s[40:41] op_sel_hi:[1,1,0]
	v_pk_fma_f32 v[178:179], v[170:171], v[178:179], s[40:41] op_sel_hi:[1,1,0]
	v_pk_fma_f32 v[180:181], v[172:173], v[180:181], s[40:41] op_sel_hi:[1,1,0]
	v_pk_fma_f32 v[182:183], v[174:175], v[182:183], s[40:41] op_sel_hi:[1,1,0]
	v_pk_fma_f32 v[176:177], v[168:169], v[176:177], s[42:43] op_sel_hi:[1,1,0]
	v_pk_fma_f32 v[178:179], v[170:171], v[178:179], s[42:43] op_sel_hi:[1,1,0]
	v_pk_fma_f32 v[180:181], v[172:173], v[180:181], s[42:43] op_sel_hi:[1,1,0]
	v_pk_fma_f32 v[182:183], v[174:175], v[182:183], s[42:43] op_sel_hi:[1,1,0]
	v_pk_fma_f32 v[176:177], v[168:169], v[176:177], s[44:45] op_sel_hi:[1,1,0]
	v_pk_fma_f32 v[178:179], v[170:171], v[178:179], s[44:45] op_sel_hi:[1,1,0]
	v_pk_fma_f32 v[180:181], v[172:173], v[180:181], s[44:45] op_sel_hi:[1,1,0]
	v_pk_fma_f32 v[182:183], v[174:175], v[182:183], s[44:45] op_sel_hi:[1,1,0]
	v_pk_fma_f32 v[168:169], v[168:169], v[176:177], s[48:49] op_sel_hi:[1,1,0]
	v_pk_fma_f32 v[170:171], v[170:171], v[178:179], s[48:49] op_sel_hi:[1,1,0]
	v_pk_fma_f32 v[172:173], v[172:173], v[180:181], s[48:49] op_sel_hi:[1,1,0]
	v_pk_fma_f32 v[174:175], v[174:175], v[182:183], s[48:49] op_sel_hi:[1,1,0]
	v_pk_fma_f32 v[160:161], v[160:161], v[168:169], 0.5 op_sel_hi:[1,1,0]
	v_pk_fma_f32 v[162:163], v[162:163], v[170:171], 0.5 op_sel_hi:[1,1,0]
	v_pk_fma_f32 v[164:165], v[164:165], v[172:173], 0.5 op_sel_hi:[1,1,0]
	v_pk_fma_f32 v[166:167], v[166:167], v[174:175], 0.5 op_sel_hi:[1,1,0]
	v_pk_mul_f32 v[44:45], v[44:45], v[160:161]
	v_pk_mul_f32 v[46:47], v[46:47], v[162:163]
	v_pk_mul_f32 v[40:41], v[40:41], v[164:165]
	v_pk_mul_f32 v[42:43], v[42:43], v[166:167]
	v_cvt_pk_bf16_f32 v184, v44, v45
	v_cvt_pk_bf16_f32 v185, v46, v47
	v_cvt_pk_bf16_f32 v186, v40, v41
	v_cvt_pk_bf16_f32 v187, v42, v43
	global_store_dwordx4 v[196:197], v[184:187], off
	v_pk_add_f32 v[36:37], v[36:37], v[60:61]
	v_pk_add_f32 v[38:39], v[38:39], v[62:63]
	v_pk_add_f32 v[32:33], v[32:33], v[56:57]
	v_pk_add_f32 v[34:35], v[34:35], v[58:59]
	v_med3_f32 v160, v36, s78, v158
	v_med3_f32 v161, v37, s78, v158
	v_med3_f32 v162, v38, s78, v158
	v_med3_f32 v163, v39, s78, v158
	v_med3_f32 v164, v32, s78, v158
	v_med3_f32 v165, v33, s78, v158
	v_med3_f32 v166, v34, s78, v158
	v_med3_f32 v167, v35, s78, v158
	v_pk_mul_f32 v[168:169], v[160:161], v[160:161]
	v_pk_mul_f32 v[170:171], v[162:163], v[162:163]
	v_pk_mul_f32 v[172:173], v[164:165], v[164:165]
	v_pk_mul_f32 v[174:175], v[166:167], v[166:167]
	v_pk_fma_f32 v[168:169], v[168:169], s[20:21], -1.0 op_sel_hi:[1,0,0]
	v_pk_fma_f32 v[170:171], v[170:171], s[20:21], -1.0 op_sel_hi:[1,0,0]
	v_pk_fma_f32 v[172:173], v[172:173], s[20:21], -1.0 op_sel_hi:[1,0,0]
	v_pk_fma_f32 v[174:175], v[174:175], s[20:21], -1.0 op_sel_hi:[1,0,0]
	v_pk_fma_f32 v[176:177], v[168:169], s[22:23], v[150:151] op_sel_hi:[1,0,0] neg_lo:[1,0,0] neg_hi:[1,0,0]
	v_pk_fma_f32 v[178:179], v[170:171], s[22:23], v[150:151] op_sel_hi:[1,0,0] neg_lo:[1,0,0] neg_hi:[1,0,0]
	v_pk_fma_f32 v[180:181], v[172:173], s[22:23], v[150:151] op_sel_hi:[1,0,0] neg_lo:[1,0,0] neg_hi:[1,0,0]
	v_pk_fma_f32 v[182:183], v[174:175], s[22:23], v[150:151] op_sel_hi:[1,0,0] neg_lo:[1,0,0] neg_hi:[1,0,0]
	v_pk_fma_f32 v[176:177], v[168:169], v[176:177], s[26:27] op_sel_hi:[1,1,0]
	v_pk_fma_f32 v[178:179], v[170:171], v[178:179], s[26:27] op_sel_hi:[1,1,0]
	v_pk_fma_f32 v[180:181], v[172:173], v[180:181], s[26:27] op_sel_hi:[1,1,0]
	v_pk_fma_f32 v[182:183], v[174:175], v[182:183], s[26:27] op_sel_hi:[1,1,0]
	v_pk_fma_f32 v[176:177], v[168:169], v[176:177], s[28:29] op_sel_hi:[1,1,0]
	v_pk_fma_f32 v[178:179], v[170:171], v[178:179], s[28:29] op_sel_hi:[1,1,0]
	v_pk_fma_f32 v[180:181], v[172:173], v[180:181], s[28:29] op_sel_hi:[1,1,0]
	v_pk_fma_f32 v[182:183], v[174:175], v[182:183], s[28:29] op_sel_hi:[1,1,0]
	v_pk_fma_f32 v[176:177], v[168:169], v[176:177], s[30:31] op_sel_hi:[1,1,0]
	v_pk_fma_f32 v[178:179], v[170:171], v[178:179], s[30:31] op_sel_hi:[1,1,0]
	v_pk_fma_f32 v[180:181], v[172:173], v[180:181], s[30:31] op_sel_hi:[1,1,0]
	v_pk_fma_f32 v[182:183], v[174:175], v[182:183], s[30:31] op_sel_hi:[1,1,0]
	v_pk_fma_f32 v[176:177], v[168:169], v[176:177], s[34:35] op_sel_hi:[1,1,0]
	v_pk_fma_f32 v[178:179], v[170:171], v[178:179], s[34:35] op_sel_hi:[1,1,0]
	v_pk_fma_f32 v[180:181], v[172:173], v[180:181], s[34:35] op_sel_hi:[1,1,0]
	v_pk_fma_f32 v[182:183], v[174:175], v[182:183], s[34:35] op_sel_hi:[1,1,0]
	v_pk_fma_f32 v[176:177], v[168:169], v[176:177], s[36:37] op_sel_hi:[1,1,0]
	v_pk_fma_f32 v[178:179], v[170:171], v[178:179], s[36:37] op_sel_hi:[1,1,0]
	v_pk_fma_f32 v[180:181], v[172:173], v[180:181], s[36:37] op_sel_hi:[1,1,0]
	v_pk_fma_f32 v[182:183], v[174:175], v[182:183], s[36:37] op_sel_hi:[1,1,0]
	v_pk_fma_f32 v[176:177], v[168:169], v[176:177], s[38:39] op_sel_hi:[1,1,0]
	v_pk_fma_f32 v[178:179], v[170:171], v[178:179], s[38:39] op_sel_hi:[1,1,0]
	v_pk_fma_f32 v[180:181], v[172:173], v[180:181], s[38:39] op_sel_hi:[1,1,0]
	v_pk_fma_f32 v[182:183], v[174:175], v[182:183], s[38:39] op_sel_hi:[1,1,0]
	v_pk_fma_f32 v[176:177], v[168:169], v[176:177], s[40:41] op_sel_hi:[1,1,0]
	v_pk_fma_f32 v[178:179], v[170:171], v[178:179], s[40:41] op_sel_hi:[1,1,0]
	v_pk_fma_f32 v[180:181], v[172:173], v[180:181], s[40:41] op_sel_hi:[1,1,0]
	v_pk_fma_f32 v[182:183], v[174:175], v[182:183], s[40:41] op_sel_hi:[1,1,0]
	v_pk_fma_f32 v[176:177], v[168:169], v[176:177], s[42:43] op_sel_hi:[1,1,0]
	v_pk_fma_f32 v[178:179], v[170:171], v[178:179], s[42:43] op_sel_hi:[1,1,0]
	v_pk_fma_f32 v[180:181], v[172:173], v[180:181], s[42:43] op_sel_hi:[1,1,0]
	v_pk_fma_f32 v[182:183], v[174:175], v[182:183], s[42:43] op_sel_hi:[1,1,0]
	v_pk_fma_f32 v[176:177], v[168:169], v[176:177], s[44:45] op_sel_hi:[1,1,0]
	v_pk_fma_f32 v[178:179], v[170:171], v[178:179], s[44:45] op_sel_hi:[1,1,0]
	v_pk_fma_f32 v[180:181], v[172:173], v[180:181], s[44:45] op_sel_hi:[1,1,0]
	v_pk_fma_f32 v[182:183], v[174:175], v[182:183], s[44:45] op_sel_hi:[1,1,0]
	v_pk_fma_f32 v[168:169], v[168:169], v[176:177], s[48:49] op_sel_hi:[1,1,0]
	v_pk_fma_f32 v[170:171], v[170:171], v[178:179], s[48:49] op_sel_hi:[1,1,0]
	v_pk_fma_f32 v[172:173], v[172:173], v[180:181], s[48:49] op_sel_hi:[1,1,0]
	v_pk_fma_f32 v[174:175], v[174:175], v[182:183], s[48:49] op_sel_hi:[1,1,0]
	v_pk_fma_f32 v[160:161], v[160:161], v[168:169], 0.5 op_sel_hi:[1,1,0]
	v_pk_fma_f32 v[162:163], v[162:163], v[170:171], 0.5 op_sel_hi:[1,1,0]
	v_pk_fma_f32 v[164:165], v[164:165], v[172:173], 0.5 op_sel_hi:[1,1,0]
	v_pk_fma_f32 v[166:167], v[166:167], v[174:175], 0.5 op_sel_hi:[1,1,0]
	v_pk_mul_f32 v[36:37], v[36:37], v[160:161]
	v_pk_mul_f32 v[38:39], v[38:39], v[162:163]
	v_pk_mul_f32 v[32:33], v[32:33], v[164:165]
	v_pk_mul_f32 v[34:35], v[34:35], v[166:167]
	v_cvt_pk_bf16_f32 v188, v36, v37
	v_cvt_pk_bf16_f32 v189, v38, v39
	v_cvt_pk_bf16_f32 v190, v32, v33
	v_cvt_pk_bf16_f32 v191, v34, v35
	global_store_dwordx4 v[196:197], v[188:191], off offset:256
	s_and_b64 vcc, exec, s[70:71]
	s_cbranch_vccz .Lg9_nostat_5
	v_pk_add_f32 v[160:161], v[44:45], v[46:47]
	v_pk_add_f32 v[162:163], v[40:41], v[42:43]
	v_pk_add_f32 v[164:165], v[36:37], v[38:39]
	v_pk_add_f32 v[166:167], v[32:33], v[34:35]
	v_pk_mul_f32 v[168:169], v[44:45], v[44:45]
	v_pk_mul_f32 v[170:171], v[36:37], v[36:37]
	v_pk_add_f32 v[160:161], v[160:161], v[162:163]
	v_pk_add_f32 v[164:165], v[164:165], v[166:167]
	v_pk_fma_f32 v[168:169], v[46:47], v[46:47], v[168:169]
	v_pk_fma_f32 v[170:171], v[38:39], v[38:39], v[170:171]
	v_pk_fma_f32 v[168:169], v[40:41], v[40:41], v[168:169]
	v_pk_fma_f32 v[170:171], v[32:33], v[32:33], v[170:171]
	v_pk_fma_f32 v[168:169], v[42:43], v[42:43], v[168:169]
	v_pk_fma_f32 v[170:171], v[34:35], v[34:35], v[170:171]
	v_pk_add_f32 v[160:161], v[160:161], v[164:165]
	v_pk_add_f32 v[168:169], v[168:169], v[170:171]
	s_nop 0
	v_add_f32_e32 v198, v160, v161
	v_add_f32_e32 v200, v168, v169
	v_mov_b32_e32 v199, v198
	s_nop 1
	v_permlane16_swap_b32 v199, v198
	s_nop 1
	v_add_f32_e32 v198, v199, v198
	v_mov_b32_e32 v202, v198
	v_mov_b32_e32 v201, v200
	s_nop 1
	v_permlane32_swap_b32 v202, v198
	s_nop 1
	s_nop 1
	v_permlane16_swap_b32 v201, v200
	s_nop 1
	v_add_f32_e32 v199, v201, v200
	v_mov_b32_e32 v203, v199
	s_nop 1
	v_permlane32_swap_b32 v203, v199
	s_nop 1
	s_and_saveexec_b64 s[4:5], s[6:7]
	v_lshlrev_b64 v[194:195], 8, v[192:193]
	v_lshl_add_u64 v[194:195], s[16:17], 0, v[194:195]
	v_lshl_add_u64 v[194:195], s[68:69], 3, v[194:195]
	v_pk_add_f32 v[200:201], v[202:203], v[198:199]
	global_store_dwordx2 v[194:195], v[200:201], off
	s_or_b64 exec, exec, s[4:5]
.Lg9_nostat_5:
	v_add_u32_e32 v192, 0xa0, v148
	v_ashrrev_i32_e32 v193, 31, v192
	v_lshlrev_b64 v[194:195], 12, v[192:193]
	v_lshl_add_u64 v[196:197], v[146:147], 0, v[194:195]
	v_pk_add_f32 v[28:29], v[28:29], v[76:77]
	v_pk_add_f32 v[30:31], v[30:31], v[78:79]
	v_pk_add_f32 v[24:25], v[24:25], v[68:69]
	v_pk_add_f32 v[26:27], v[26:27], v[70:71]
	v_med3_f32 v160, v28, s78, v158
	v_med3_f32 v161, v29, s78, v158
	v_med3_f32 v162, v30, s78, v158
	v_med3_f32 v163, v31, s78, v158
	v_med3_f32 v164, v24, s78, v158
	v_med3_f32 v165, v25, s78, v158
	v_med3_f32 v166, v26, s78, v158
	v_med3_f32 v167, v27, s78, v158
	v_pk_mul_f32 v[168:169], v[160:161], v[160:161]
	v_pk_mul_f32 v[170:171], v[162:163], v[162:163]
	v_pk_mul_f32 v[172:173], v[164:165], v[164:165]
	v_pk_mul_f32 v[174:175], v[166:167], v[166:167]
	v_pk_fma_f32 v[168:169], v[168:169], s[20:21], -1.0 op_sel_hi:[1,0,0]
	v_pk_fma_f32 v[170:171], v[170:171], s[20:21], -1.0 op_sel_hi:[1,0,0]
	v_pk_fma_f32 v[172:173], v[172:173], s[20:21], -1.0 op_sel_hi:[1,0,0]
	v_pk_fma_f32 v[174:175], v[174:175], s[20:21], -1.0 op_sel_hi:[1,0,0]
	v_pk_fma_f32 v[176:177], v[168:169], s[22:23], v[150:151] op_sel_hi:[1,0,0] neg_lo:[1,0,0] neg_hi:[1,0,0]
	v_pk_fma_f32 v[178:179], v[170:171], s[22:23], v[150:151] op_sel_hi:[1,0,0] neg_lo:[1,0,0] neg_hi:[1,0,0]
	v_pk_fma_f32 v[180:181], v[172:173], s[22:23], v[150:151] op_sel_hi:[1,0,0] neg_lo:[1,0,0] neg_hi:[1,0,0]
	v_pk_fma_f32 v[182:183], v[174:175], s[22:23], v[150:151] op_sel_hi:[1,0,0] neg_lo:[1,0,0] neg_hi:[1,0,0]
	v_pk_fma_f32 v[176:177], v[168:169], v[176:177], s[26:27] op_sel_hi:[1,1,0]
	v_pk_fma_f32 v[178:179], v[170:171], v[178:179], s[26:27] op_sel_hi:[1,1,0]
	v_pk_fma_f32 v[180:181], v[172:173], v[180:181], s[26:27] op_sel_hi:[1,1,0]
	v_pk_fma_f32 v[182:183], v[174:175], v[182:183], s[26:27] op_sel_hi:[1,1,0]
	v_pk_fma_f32 v[176:177], v[168:169], v[176:177], s[28:29] op_sel_hi:[1,1,0]
	v_pk_fma_f32 v[178:179], v[170:171], v[178:179], s[28:29] op_sel_hi:[1,1,0]
	v_pk_fma_f32 v[180:181], v[172:173], v[180:181], s[28:29] op_sel_hi:[1,1,0]
	v_pk_fma_f32 v[182:183], v[174:175], v[182:183], s[28:29] op_sel_hi:[1,1,0]
	v_pk_fma_f32 v[176:177], v[168:169], v[176:177], s[30:31] op_sel_hi:[1,1,0]
	v_pk_fma_f32 v[178:179], v[170:171], v[178:179], s[30:31] op_sel_hi:[1,1,0]
	v_pk_fma_f32 v[180:181], v[172:173], v[180:181], s[30:31] op_sel_hi:[1,1,0]
	v_pk_fma_f32 v[182:183], v[174:175], v[182:183], s[30:31] op_sel_hi:[1,1,0]
	v_pk_fma_f32 v[176:177], v[168:169], v[176:177], s[34:35] op_sel_hi:[1,1,0]
	v_pk_fma_f32 v[178:179], v[170:171], v[178:179], s[34:35] op_sel_hi:[1,1,0]
	v_pk_fma_f32 v[180:181], v[172:173], v[180:181], s[34:35] op_sel_hi:[1,1,0]
	v_pk_fma_f32 v[182:183], v[174:175], v[182:183], s[34:35] op_sel_hi:[1,1,0]
	v_pk_fma_f32 v[176:177], v[168:169], v[176:177], s[36:37] op_sel_hi:[1,1,0]
	v_pk_fma_f32 v[178:179], v[170:171], v[178:179], s[36:37] op_sel_hi:[1,1,0]
	v_pk_fma_f32 v[180:181], v[172:173], v[180:181], s[36:37] op_sel_hi:[1,1,0]
	v_pk_fma_f32 v[182:183], v[174:175], v[182:183], s[36:37] op_sel_hi:[1,1,0]
	v_pk_fma_f32 v[176:177], v[168:169], v[176:177], s[38:39] op_sel_hi:[1,1,0]
	v_pk_fma_f32 v[178:179], v[170:171], v[178:179], s[38:39] op_sel_hi:[1,1,0]
	v_pk_fma_f32 v[180:181], v[172:173], v[180:181], s[38:39] op_sel_hi:[1,1,0]
	v_pk_fma_f32 v[182:183], v[174:175], v[182:183], s[38:39] op_sel_hi:[1,1,0]
	v_pk_fma_f32 v[176:177], v[168:169], v[176:177], s[40:41] op_sel_hi:[1,1,0]
	v_pk_fma_f32 v[178:179], v[170:171], v[178:179], s[40:41] op_sel_hi:[1,1,0]
	v_pk_fma_f32 v[180:181], v[172:173], v[180:181], s[40:41] op_sel_hi:[1,1,0]
	v_pk_fma_f32 v[182:183], v[174:175], v[182:183], s[40:41] op_sel_hi:[1,1,0]
	v_pk_fma_f32 v[176:177], v[168:169], v[176:177], s[42:43] op_sel_hi:[1,1,0]
	v_pk_fma_f32 v[178:179], v[170:171], v[178:179], s[42:43] op_sel_hi:[1,1,0]
	v_pk_fma_f32 v[180:181], v[172:173], v[180:181], s[42:43] op_sel_hi:[1,1,0]
	v_pk_fma_f32 v[182:183], v[174:175], v[182:183], s[42:43] op_sel_hi:[1,1,0]
	v_pk_fma_f32 v[176:177], v[168:169], v[176:177], s[44:45] op_sel_hi:[1,1,0]
	v_pk_fma_f32 v[178:179], v[170:171], v[178:179], s[44:45] op_sel_hi:[1,1,0]
	v_pk_fma_f32 v[180:181], v[172:173], v[180:181], s[44:45] op_sel_hi:[1,1,0]
	v_pk_fma_f32 v[182:183], v[174:175], v[182:183], s[44:45] op_sel_hi:[1,1,0]
	v_pk_fma_f32 v[168:169], v[168:169], v[176:177], s[48:49] op_sel_hi:[1,1,0]
	v_pk_fma_f32 v[170:171], v[170:171], v[178:179], s[48:49] op_sel_hi:[1,1,0]
	v_pk_fma_f32 v[172:173], v[172:173], v[180:181], s[48:49] op_sel_hi:[1,1,0]
	v_pk_fma_f32 v[174:175], v[174:175], v[182:183], s[48:49] op_sel_hi:[1,1,0]
	v_pk_fma_f32 v[160:161], v[160:161], v[168:169], 0.5 op_sel_hi:[1,1,0]
	v_pk_fma_f32 v[162:163], v[162:163], v[170:171], 0.5 op_sel_hi:[1,1,0]
	v_pk_fma_f32 v[164:165], v[164:165], v[172:173], 0.5 op_sel_hi:[1,1,0]
	v_pk_fma_f32 v[166:167], v[166:167], v[174:175], 0.5 op_sel_hi:[1,1,0]
	v_pk_mul_f32 v[28:29], v[28:29], v[160:161]
	v_pk_mul_f32 v[30:31], v[30:31], v[162:163]
	v_pk_mul_f32 v[24:25], v[24:25], v[164:165]
	v_pk_mul_f32 v[26:27], v[26:27], v[166:167]
	v_cvt_pk_bf16_f32 v184, v28, v29
	v_cvt_pk_bf16_f32 v185, v30, v31
	v_cvt_pk_bf16_f32 v186, v24, v25
	v_cvt_pk_bf16_f32 v187, v26, v27
	global_store_dwordx4 v[196:197], v[184:187], off
	v_pk_add_f32 v[20:21], v[20:21], v[60:61]
	v_pk_add_f32 v[22:23], v[22:23], v[62:63]
	v_pk_add_f32 v[16:17], v[16:17], v[56:57]
	v_pk_add_f32 v[18:19], v[18:19], v[58:59]
	v_med3_f32 v160, v20, s78, v158
	v_med3_f32 v161, v21, s78, v158
	v_med3_f32 v162, v22, s78, v158
	v_med3_f32 v163, v23, s78, v158
	v_med3_f32 v164, v16, s78, v158
	v_med3_f32 v165, v17, s78, v158
	v_med3_f32 v166, v18, s78, v158
	v_med3_f32 v167, v19, s78, v158
	v_pk_mul_f32 v[168:169], v[160:161], v[160:161]
	v_pk_mul_f32 v[170:171], v[162:163], v[162:163]
	v_pk_mul_f32 v[172:173], v[164:165], v[164:165]
	v_pk_mul_f32 v[174:175], v[166:167], v[166:167]
	v_pk_fma_f32 v[168:169], v[168:169], s[20:21], -1.0 op_sel_hi:[1,0,0]
	v_pk_fma_f32 v[170:171], v[170:171], s[20:21], -1.0 op_sel_hi:[1,0,0]
	v_pk_fma_f32 v[172:173], v[172:173], s[20:21], -1.0 op_sel_hi:[1,0,0]
	v_pk_fma_f32 v[174:175], v[174:175], s[20:21], -1.0 op_sel_hi:[1,0,0]
	v_pk_fma_f32 v[176:177], v[168:169], s[22:23], v[150:151] op_sel_hi:[1,0,0] neg_lo:[1,0,0] neg_hi:[1,0,0]
	v_pk_fma_f32 v[178:179], v[170:171], s[22:23], v[150:151] op_sel_hi:[1,0,0] neg_lo:[1,0,0] neg_hi:[1,0,0]
	v_pk_fma_f32 v[180:181], v[172:173], s[22:23], v[150:151] op_sel_hi:[1,0,0] neg_lo:[1,0,0] neg_hi:[1,0,0]
	v_pk_fma_f32 v[182:183], v[174:175], s[22:23], v[150:151] op_sel_hi:[1,0,0] neg_lo:[1,0,0] neg_hi:[1,0,0]
	v_pk_fma_f32 v[176:177], v[168:169], v[176:177], s[26:27] op_sel_hi:[1,1,0]
	v_pk_fma_f32 v[178:179], v[170:171], v[178:179], s[26:27] op_sel_hi:[1,1,0]
	v_pk_fma_f32 v[180:181], v[172:173], v[180:181], s[26:27] op_sel_hi:[1,1,0]
	v_pk_fma_f32 v[182:183], v[174:175], v[182:183], s[26:27] op_sel_hi:[1,1,0]
	v_pk_fma_f32 v[176:177], v[168:169], v[176:177], s[28:29] op_sel_hi:[1,1,0]
	v_pk_fma_f32 v[178:179], v[170:171], v[178:179], s[28:29] op_sel_hi:[1,1,0]
	v_pk_fma_f32 v[180:181], v[172:173], v[180:181], s[28:29] op_sel_hi:[1,1,0]
	v_pk_fma_f32 v[182:183], v[174:175], v[182:183], s[28:29] op_sel_hi:[1,1,0]
	v_pk_fma_f32 v[176:177], v[168:169], v[176:177], s[30:31] op_sel_hi:[1,1,0]
	v_pk_fma_f32 v[178:179], v[170:171], v[178:179], s[30:31] op_sel_hi:[1,1,0]
	v_pk_fma_f32 v[180:181], v[172:173], v[180:181], s[30:31] op_sel_hi:[1,1,0]
	v_pk_fma_f32 v[182:183], v[174:175], v[182:183], s[30:31] op_sel_hi:[1,1,0]
	v_pk_fma_f32 v[176:177], v[168:169], v[176:177], s[34:35] op_sel_hi:[1,1,0]
	v_pk_fma_f32 v[178:179], v[170:171], v[178:179], s[34:35] op_sel_hi:[1,1,0]
	v_pk_fma_f32 v[180:181], v[172:173], v[180:181], s[34:35] op_sel_hi:[1,1,0]
	v_pk_fma_f32 v[182:183], v[174:175], v[182:183], s[34:35] op_sel_hi:[1,1,0]
	v_pk_fma_f32 v[176:177], v[168:169], v[176:177], s[36:37] op_sel_hi:[1,1,0]
	v_pk_fma_f32 v[178:179], v[170:171], v[178:179], s[36:37] op_sel_hi:[1,1,0]
	v_pk_fma_f32 v[180:181], v[172:173], v[180:181], s[36:37] op_sel_hi:[1,1,0]
	v_pk_fma_f32 v[182:183], v[174:175], v[182:183], s[36:37] op_sel_hi:[1,1,0]
	v_pk_fma_f32 v[176:177], v[168:169], v[176:177], s[38:39] op_sel_hi:[1,1,0]
	v_pk_fma_f32 v[178:179], v[170:171], v[178:179], s[38:39] op_sel_hi:[1,1,0]
	v_pk_fma_f32 v[180:181], v[172:173], v[180:181], s[38:39] op_sel_hi:[1,1,0]
	v_pk_fma_f32 v[182:183], v[174:175], v[182:183], s[38:39] op_sel_hi:[1,1,0]
	v_pk_fma_f32 v[176:177], v[168:169], v[176:177], s[40:41] op_sel_hi:[1,1,0]
	v_pk_fma_f32 v[178:179], v[170:171], v[178:179], s[40:41] op_sel_hi:[1,1,0]
	v_pk_fma_f32 v[180:181], v[172:173], v[180:181], s[40:41] op_sel_hi:[1,1,0]
	v_pk_fma_f32 v[182:183], v[174:175], v[182:183], s[40:41] op_sel_hi:[1,1,0]
	v_pk_fma_f32 v[176:177], v[168:169], v[176:177], s[42:43] op_sel_hi:[1,1,0]
	v_pk_fma_f32 v[178:179], v[170:171], v[178:179], s[42:43] op_sel_hi:[1,1,0]
	v_pk_fma_f32 v[180:181], v[172:173], v[180:181], s[42:43] op_sel_hi:[1,1,0]
	v_pk_fma_f32 v[182:183], v[174:175], v[182:183], s[42:43] op_sel_hi:[1,1,0]
	v_pk_fma_f32 v[176:177], v[168:169], v[176:177], s[44:45] op_sel_hi:[1,1,0]
	v_pk_fma_f32 v[178:179], v[170:171], v[178:179], s[44:45] op_sel_hi:[1,1,0]
	v_pk_fma_f32 v[180:181], v[172:173], v[180:181], s[44:45] op_sel_hi:[1,1,0]
	v_pk_fma_f32 v[182:183], v[174:175], v[182:183], s[44:45] op_sel_hi:[1,1,0]
	v_pk_fma_f32 v[168:169], v[168:169], v[176:177], s[48:49] op_sel_hi:[1,1,0]
	v_pk_fma_f32 v[170:171], v[170:171], v[178:179], s[48:49] op_sel_hi:[1,1,0]
	v_pk_fma_f32 v[172:173], v[172:173], v[180:181], s[48:49] op_sel_hi:[1,1,0]
	v_pk_fma_f32 v[174:175], v[174:175], v[182:183], s[48:49] op_sel_hi:[1,1,0]
	v_pk_fma_f32 v[160:161], v[160:161], v[168:169], 0.5 op_sel_hi:[1,1,0]
	v_pk_fma_f32 v[162:163], v[162:163], v[170:171], 0.5 op_sel_hi:[1,1,0]
	v_pk_fma_f32 v[164:165], v[164:165], v[172:173], 0.5 op_sel_hi:[1,1,0]
	v_pk_fma_f32 v[166:167], v[166:167], v[174:175], 0.5 op_sel_hi:[1,1,0]
	v_pk_mul_f32 v[20:21], v[20:21], v[160:161]
	v_pk_mul_f32 v[22:23], v[22:23], v[162:163]
	v_pk_mul_f32 v[16:17], v[16:17], v[164:165]
	v_pk_mul_f32 v[18:19], v[18:19], v[166:167]
	v_cvt_pk_bf16_f32 v188, v20, v21
	v_cvt_pk_bf16_f32 v189, v22, v23
	v_cvt_pk_bf16_f32 v190, v16, v17
	v_cvt_pk_bf16_f32 v191, v18, v19
	global_store_dwordx4 v[196:197], v[188:191], off offset:256
	s_and_b64 vcc, exec, s[70:71]
	s_cbranch_vccz .Lg9_nostat_6
	v_pk_add_f32 v[160:161], v[28:29], v[30:31]
	v_pk_add_f32 v[162:163], v[24:25], v[26:27]
	v_pk_add_f32 v[164:165], v[20:21], v[22:23]
	v_pk_add_f32 v[166:167], v[16:17], v[18:19]
	v_pk_mul_f32 v[168:169], v[28:29], v[28:29]
	v_pk_mul_f32 v[170:171], v[20:21], v[20:21]
	v_pk_add_f32 v[160:161], v[160:161], v[162:163]
	v_pk_add_f32 v[164:165], v[164:165], v[166:167]
	v_pk_fma_f32 v[168:169], v[30:31], v[30:31], v[168:169]
	v_pk_fma_f32 v[170:171], v[22:23], v[22:23], v[170:171]
	v_pk_fma_f32 v[168:169], v[24:25], v[24:25], v[168:169]
	v_pk_fma_f32 v[170:171], v[16:17], v[16:17], v[170:171]
	v_pk_fma_f32 v[168:169], v[26:27], v[26:27], v[168:169]
	v_pk_fma_f32 v[170:171], v[18:19], v[18:19], v[170:171]
	v_pk_add_f32 v[160:161], v[160:161], v[164:165]
	v_pk_add_f32 v[168:169], v[168:169], v[170:171]
	s_nop 0
	v_add_f32_e32 v198, v160, v161
	v_add_f32_e32 v200, v168, v169
	v_mov_b32_e32 v199, v198
	s_nop 1
	v_permlane16_swap_b32 v199, v198
	s_nop 1
	v_add_f32_e32 v198, v199, v198
	v_mov_b32_e32 v202, v198
	v_mov_b32_e32 v201, v200
	s_nop 1
	v_permlane32_swap_b32 v202, v198
	s_nop 1
	s_nop 1
	v_permlane16_swap_b32 v201, v200
	s_nop 1
	v_add_f32_e32 v199, v201, v200
	v_mov_b32_e32 v203, v199
	s_nop 1
	v_permlane32_swap_b32 v203, v199
	s_nop 1
	s_and_saveexec_b64 s[4:5], s[6:7]
	v_lshlrev_b64 v[194:195], 8, v[192:193]
	v_lshl_add_u64 v[194:195], s[16:17], 0, v[194:195]
	v_lshl_add_u64 v[194:195], s[68:69], 3, v[194:195]
	v_pk_add_f32 v[200:201], v[202:203], v[198:199]
	global_store_dwordx2 v[194:195], v[200:201], off
	s_or_b64 exec, exec, s[4:5]
.Lg9_nostat_6:
	v_add_u32_e32 v192, 0xb0, v148
	v_ashrrev_i32_e32 v193, 31, v192
	v_lshlrev_b64 v[194:195], 12, v[192:193]
	v_lshl_add_u64 v[196:197], v[146:147], 0, v[194:195]
	v_pk_add_f32 v[12:13], v[12:13], v[76:77]
	v_pk_add_f32 v[14:15], v[14:15], v[78:79]
	v_pk_add_f32 v[8:9], v[8:9], v[68:69]
	v_pk_add_f32 v[10:11], v[10:11], v[70:71]
	v_med3_f32 v160, v12, s78, v158
	v_med3_f32 v161, v13, s78, v158
	v_med3_f32 v162, v14, s78, v158
	v_med3_f32 v163, v15, s78, v158
	v_med3_f32 v164, v8, s78, v158
	v_med3_f32 v165, v9, s78, v158
	v_med3_f32 v166, v10, s78, v158
	v_med3_f32 v167, v11, s78, v158
	v_pk_mul_f32 v[168:169], v[160:161], v[160:161]
	v_pk_mul_f32 v[170:171], v[162:163], v[162:163]
	v_pk_mul_f32 v[172:173], v[164:165], v[164:165]
	v_pk_mul_f32 v[174:175], v[166:167], v[166:167]
	v_pk_fma_f32 v[168:169], v[168:169], s[20:21], -1.0 op_sel_hi:[1,0,0]
	v_pk_fma_f32 v[170:171], v[170:171], s[20:21], -1.0 op_sel_hi:[1,0,0]
	v_pk_fma_f32 v[172:173], v[172:173], s[20:21], -1.0 op_sel_hi:[1,0,0]
	v_pk_fma_f32 v[174:175], v[174:175], s[20:21], -1.0 op_sel_hi:[1,0,0]
	v_pk_fma_f32 v[176:177], v[168:169], s[22:23], v[150:151] op_sel_hi:[1,0,0] neg_lo:[1,0,0] neg_hi:[1,0,0]
	v_pk_fma_f32 v[178:179], v[170:171], s[22:23], v[150:151] op_sel_hi:[1,0,0] neg_lo:[1,0,0] neg_hi:[1,0,0]
	v_pk_fma_f32 v[180:181], v[172:173], s[22:23], v[150:151] op_sel_hi:[1,0,0] neg_lo:[1,0,0] neg_hi:[1,0,0]
	v_pk_fma_f32 v[182:183], v[174:175], s[22:23], v[150:151] op_sel_hi:[1,0,0] neg_lo:[1,0,0] neg_hi:[1,0,0]
	v_pk_fma_f32 v[176:177], v[168:169], v[176:177], s[26:27] op_sel_hi:[1,1,0]
	v_pk_fma_f32 v[178:179], v[170:171], v[178:179], s[26:27] op_sel_hi:[1,1,0]
	v_pk_fma_f32 v[180:181], v[172:173], v[180:181], s[26:27] op_sel_hi:[1,1,0]
	v_pk_fma_f32 v[182:183], v[174:175], v[182:183], s[26:27] op_sel_hi:[1,1,0]
	v_pk_fma_f32 v[176:177], v[168:169], v[176:177], s[28:29] op_sel_hi:[1,1,0]
	v_pk_fma_f32 v[178:179], v[170:171], v[178:179], s[28:29] op_sel_hi:[1,1,0]
	v_pk_fma_f32 v[180:181], v[172:173], v[180:181], s[28:29] op_sel_hi:[1,1,0]
	v_pk_fma_f32 v[182:183], v[174:175], v[182:183], s[28:29] op_sel_hi:[1,1,0]
	v_pk_fma_f32 v[176:177], v[168:169], v[176:177], s[30:31] op_sel_hi:[1,1,0]
	v_pk_fma_f32 v[178:179], v[170:171], v[178:179], s[30:31] op_sel_hi:[1,1,0]
	v_pk_fma_f32 v[180:181], v[172:173], v[180:181], s[30:31] op_sel_hi:[1,1,0]
	v_pk_fma_f32 v[182:183], v[174:175], v[182:183], s[30:31] op_sel_hi:[1,1,0]
	v_pk_fma_f32 v[176:177], v[168:169], v[176:177], s[34:35] op_sel_hi:[1,1,0]
	v_pk_fma_f32 v[178:179], v[170:171], v[178:179], s[34:35] op_sel_hi:[1,1,0]
	v_pk_fma_f32 v[180:181], v[172:173], v[180:181], s[34:35] op_sel_hi:[1,1,0]
	v_pk_fma_f32 v[182:183], v[174:175], v[182:183], s[34:35] op_sel_hi:[1,1,0]
	v_pk_fma_f32 v[176:177], v[168:169], v[176:177], s[36:37] op_sel_hi:[1,1,0]
	v_pk_fma_f32 v[178:179], v[170:171], v[178:179], s[36:37] op_sel_hi:[1,1,0]
	v_pk_fma_f32 v[180:181], v[172:173], v[180:181], s[36:37] op_sel_hi:[1,1,0]
	v_pk_fma_f32 v[182:183], v[174:175], v[182:183], s[36:37] op_sel_hi:[1,1,0]
	v_pk_fma_f32 v[176:177], v[168:169], v[176:177], s[38:39] op_sel_hi:[1,1,0]
	v_pk_fma_f32 v[178:179], v[170:171], v[178:179], s[38:39] op_sel_hi:[1,1,0]
	v_pk_fma_f32 v[180:181], v[172:173], v[180:181], s[38:39] op_sel_hi:[1,1,0]
	v_pk_fma_f32 v[182:183], v[174:175], v[182:183], s[38:39] op_sel_hi:[1,1,0]
	v_pk_fma_f32 v[176:177], v[168:169], v[176:177], s[40:41] op_sel_hi:[1,1,0]
	v_pk_fma_f32 v[178:179], v[170:171], v[178:179], s[40:41] op_sel_hi:[1,1,0]
	v_pk_fma_f32 v[180:181], v[172:173], v[180:181], s[40:41] op_sel_hi:[1,1,0]
	v_pk_fma_f32 v[182:183], v[174:175], v[182:183], s[40:41] op_sel_hi:[1,1,0]
	v_pk_fma_f32 v[176:177], v[168:169], v[176:177], s[42:43] op_sel_hi:[1,1,0]
	v_pk_fma_f32 v[178:179], v[170:171], v[178:179], s[42:43] op_sel_hi:[1,1,0]
	v_pk_fma_f32 v[180:181], v[172:173], v[180:181], s[42:43] op_sel_hi:[1,1,0]
	v_pk_fma_f32 v[182:183], v[174:175], v[182:183], s[42:43] op_sel_hi:[1,1,0]
	v_pk_fma_f32 v[176:177], v[168:169], v[176:177], s[44:45] op_sel_hi:[1,1,0]
	v_pk_fma_f32 v[178:179], v[170:171], v[178:179], s[44:45] op_sel_hi:[1,1,0]
	v_pk_fma_f32 v[180:181], v[172:173], v[180:181], s[44:45] op_sel_hi:[1,1,0]
	v_pk_fma_f32 v[182:183], v[174:175], v[182:183], s[44:45] op_sel_hi:[1,1,0]
	v_pk_fma_f32 v[168:169], v[168:169], v[176:177], s[48:49] op_sel_hi:[1,1,0]
	v_pk_fma_f32 v[170:171], v[170:171], v[178:179], s[48:49] op_sel_hi:[1,1,0]
	v_pk_fma_f32 v[172:173], v[172:173], v[180:181], s[48:49] op_sel_hi:[1,1,0]
	v_pk_fma_f32 v[174:175], v[174:175], v[182:183], s[48:49] op_sel_hi:[1,1,0]
	v_pk_fma_f32 v[160:161], v[160:161], v[168:169], 0.5 op_sel_hi:[1,1,0]
	v_pk_fma_f32 v[162:163], v[162:163], v[170:171], 0.5 op_sel_hi:[1,1,0]
	v_pk_fma_f32 v[164:165], v[164:165], v[172:173], 0.5 op_sel_hi:[1,1,0]
	v_pk_fma_f32 v[166:167], v[166:167], v[174:175], 0.5 op_sel_hi:[1,1,0]
	v_pk_mul_f32 v[12:13], v[12:13], v[160:161]
	v_pk_mul_f32 v[14:15], v[14:15], v[162:163]
	v_pk_mul_f32 v[8:9], v[8:9], v[164:165]
	v_pk_mul_f32 v[10:11], v[10:11], v[166:167]
	v_cvt_pk_bf16_f32 v184, v12, v13
	v_cvt_pk_bf16_f32 v185, v14, v15
	v_cvt_pk_bf16_f32 v186, v8, v9
	v_cvt_pk_bf16_f32 v187, v10, v11
	global_store_dwordx4 v[196:197], v[184:187], off
	v_pk_add_f32 v[4:5], v[4:5], v[60:61]
	v_pk_add_f32 v[6:7], v[6:7], v[62:63]
	v_pk_add_f32 v[0:1], v[0:1], v[56:57]
	v_pk_add_f32 v[2:3], v[2:3], v[58:59]
	v_med3_f32 v160, v4, s78, v158
	v_med3_f32 v161, v5, s78, v158
	v_med3_f32 v162, v6, s78, v158
	v_med3_f32 v163, v7, s78, v158
	v_med3_f32 v164, v0, s78, v158
	v_med3_f32 v165, v1, s78, v158
	v_med3_f32 v166, v2, s78, v158
	v_med3_f32 v167, v3, s78, v158
	v_pk_mul_f32 v[168:169], v[160:161], v[160:161]
	v_pk_mul_f32 v[170:171], v[162:163], v[162:163]
	v_pk_mul_f32 v[172:173], v[164:165], v[164:165]
	v_pk_mul_f32 v[174:175], v[166:167], v[166:167]
	v_pk_fma_f32 v[168:169], v[168:169], s[20:21], -1.0 op_sel_hi:[1,0,0]
	v_pk_fma_f32 v[170:171], v[170:171], s[20:21], -1.0 op_sel_hi:[1,0,0]
	v_pk_fma_f32 v[172:173], v[172:173], s[20:21], -1.0 op_sel_hi:[1,0,0]
	v_pk_fma_f32 v[174:175], v[174:175], s[20:21], -1.0 op_sel_hi:[1,0,0]
	v_pk_fma_f32 v[176:177], v[168:169], s[22:23], v[150:151] op_sel_hi:[1,0,0] neg_lo:[1,0,0] neg_hi:[1,0,0]
	v_pk_fma_f32 v[178:179], v[170:171], s[22:23], v[150:151] op_sel_hi:[1,0,0] neg_lo:[1,0,0] neg_hi:[1,0,0]
	v_pk_fma_f32 v[180:181], v[172:173], s[22:23], v[150:151] op_sel_hi:[1,0,0] neg_lo:[1,0,0] neg_hi:[1,0,0]
	v_pk_fma_f32 v[182:183], v[174:175], s[22:23], v[150:151] op_sel_hi:[1,0,0] neg_lo:[1,0,0] neg_hi:[1,0,0]
	v_pk_fma_f32 v[176:177], v[168:169], v[176:177], s[26:27] op_sel_hi:[1,1,0]
	v_pk_fma_f32 v[178:179], v[170:171], v[178:179], s[26:27] op_sel_hi:[1,1,0]
	v_pk_fma_f32 v[180:181], v[172:173], v[180:181], s[26:27] op_sel_hi:[1,1,0]
	v_pk_fma_f32 v[182:183], v[174:175], v[182:183], s[26:27] op_sel_hi:[1,1,0]
	v_pk_fma_f32 v[176:177], v[168:169], v[176:177], s[28:29] op_sel_hi:[1,1,0]
	v_pk_fma_f32 v[178:179], v[170:171], v[178:179], s[28:29] op_sel_hi:[1,1,0]
	v_pk_fma_f32 v[180:181], v[172:173], v[180:181], s[28:29] op_sel_hi:[1,1,0]
	v_pk_fma_f32 v[182:183], v[174:175], v[182:183], s[28:29] op_sel_hi:[1,1,0]
	v_pk_fma_f32 v[176:177], v[168:169], v[176:177], s[30:31] op_sel_hi:[1,1,0]
	v_pk_fma_f32 v[178:179], v[170:171], v[178:179], s[30:31] op_sel_hi:[1,1,0]
	v_pk_fma_f32 v[180:181], v[172:173], v[180:181], s[30:31] op_sel_hi:[1,1,0]
	v_pk_fma_f32 v[182:183], v[174:175], v[182:183], s[30:31] op_sel_hi:[1,1,0]
	v_pk_fma_f32 v[176:177], v[168:169], v[176:177], s[34:35] op_sel_hi:[1,1,0]
	v_pk_fma_f32 v[178:179], v[170:171], v[178:179], s[34:35] op_sel_hi:[1,1,0]
	v_pk_fma_f32 v[180:181], v[172:173], v[180:181], s[34:35] op_sel_hi:[1,1,0]
	v_pk_fma_f32 v[182:183], v[174:175], v[182:183], s[34:35] op_sel_hi:[1,1,0]
	v_pk_fma_f32 v[176:177], v[168:169], v[176:177], s[36:37] op_sel_hi:[1,1,0]
	v_pk_fma_f32 v[178:179], v[170:171], v[178:179], s[36:37] op_sel_hi:[1,1,0]
	v_pk_fma_f32 v[180:181], v[172:173], v[180:181], s[36:37] op_sel_hi:[1,1,0]
	v_pk_fma_f32 v[182:183], v[174:175], v[182:183], s[36:37] op_sel_hi:[1,1,0]
	v_pk_fma_f32 v[176:177], v[168:169], v[176:177], s[38:39] op_sel_hi:[1,1,0]
	v_pk_fma_f32 v[178:179], v[170:171], v[178:179], s[38:39] op_sel_hi:[1,1,0]
	v_pk_fma_f32 v[180:181], v[172:173], v[180:181], s[38:39] op_sel_hi:[1,1,0]
	v_pk_fma_f32 v[182:183], v[174:175], v[182:183], s[38:39] op_sel_hi:[1,1,0]
	v_pk_fma_f32 v[176:177], v[168:169], v[176:177], s[40:41] op_sel_hi:[1,1,0]
	v_pk_fma_f32 v[178:179], v[170:171], v[178:179], s[40:41] op_sel_hi:[1,1,0]
	v_pk_fma_f32 v[180:181], v[172:173], v[180:181], s[40:41] op_sel_hi:[1,1,0]
	v_pk_fma_f32 v[182:183], v[174:175], v[182:183], s[40:41] op_sel_hi:[1,1,0]
	v_pk_fma_f32 v[176:177], v[168:169], v[176:177], s[42:43] op_sel_hi:[1,1,0]
	v_pk_fma_f32 v[178:179], v[170:171], v[178:179], s[42:43] op_sel_hi:[1,1,0]
	v_pk_fma_f32 v[180:181], v[172:173], v[180:181], s[42:43] op_sel_hi:[1,1,0]
	v_pk_fma_f32 v[182:183], v[174:175], v[182:183], s[42:43] op_sel_hi:[1,1,0]
	v_pk_fma_f32 v[176:177], v[168:169], v[176:177], s[44:45] op_sel_hi:[1,1,0]
	v_pk_fma_f32 v[178:179], v[170:171], v[178:179], s[44:45] op_sel_hi:[1,1,0]
	v_pk_fma_f32 v[180:181], v[172:173], v[180:181], s[44:45] op_sel_hi:[1,1,0]
	v_pk_fma_f32 v[182:183], v[174:175], v[182:183], s[44:45] op_sel_hi:[1,1,0]
	v_pk_fma_f32 v[168:169], v[168:169], v[176:177], s[48:49] op_sel_hi:[1,1,0]
	v_pk_fma_f32 v[170:171], v[170:171], v[178:179], s[48:49] op_sel_hi:[1,1,0]
	v_pk_fma_f32 v[172:173], v[172:173], v[180:181], s[48:49] op_sel_hi:[1,1,0]
	v_pk_fma_f32 v[174:175], v[174:175], v[182:183], s[48:49] op_sel_hi:[1,1,0]
	v_pk_fma_f32 v[160:161], v[160:161], v[168:169], 0.5 op_sel_hi:[1,1,0]
	v_pk_fma_f32 v[162:163], v[162:163], v[170:171], 0.5 op_sel_hi:[1,1,0]
	v_pk_fma_f32 v[164:165], v[164:165], v[172:173], 0.5 op_sel_hi:[1,1,0]
	v_pk_fma_f32 v[166:167], v[166:167], v[174:175], 0.5 op_sel_hi:[1,1,0]
	v_pk_mul_f32 v[4:5], v[4:5], v[160:161]
	v_pk_mul_f32 v[6:7], v[6:7], v[162:163]
	v_pk_mul_f32 v[0:1], v[0:1], v[164:165]
	v_pk_mul_f32 v[2:3], v[2:3], v[166:167]
	v_cvt_pk_bf16_f32 v188, v4, v5
	v_cvt_pk_bf16_f32 v189, v6, v7
	v_cvt_pk_bf16_f32 v190, v0, v1
	v_cvt_pk_bf16_f32 v191, v2, v3
	global_store_dwordx4 v[196:197], v[188:191], off offset:256
	s_and_b64 vcc, exec, s[70:71]
	s_cbranch_vccz .Lg9_nostat_7
	v_pk_add_f32 v[160:161], v[12:13], v[14:15]
	v_pk_add_f32 v[162:163], v[8:9], v[10:11]
	v_pk_add_f32 v[164:165], v[4:5], v[6:7]
	v_pk_add_f32 v[166:167], v[0:1], v[2:3]
	v_pk_mul_f32 v[168:169], v[12:13], v[12:13]
	v_pk_mul_f32 v[170:171], v[4:5], v[4:5]
	v_pk_add_f32 v[160:161], v[160:161], v[162:163]
	v_pk_add_f32 v[164:165], v[164:165], v[166:167]
	v_pk_fma_f32 v[168:169], v[14:15], v[14:15], v[168:169]
	v_pk_fma_f32 v[170:171], v[6:7], v[6:7], v[170:171]
	v_pk_fma_f32 v[168:169], v[8:9], v[8:9], v[168:169]
	v_pk_fma_f32 v[170:171], v[0:1], v[0:1], v[170:171]
	v_pk_fma_f32 v[168:169], v[10:11], v[10:11], v[168:169]
	v_pk_fma_f32 v[170:171], v[2:3], v[2:3], v[170:171]
	v_pk_add_f32 v[160:161], v[160:161], v[164:165]
	v_pk_add_f32 v[168:169], v[168:169], v[170:171]
	s_nop 0
	v_add_f32_e32 v198, v160, v161
	v_add_f32_e32 v200, v168, v169
	v_mov_b32_e32 v199, v198
	s_nop 1
	v_permlane16_swap_b32 v199, v198
	s_nop 1
	v_add_f32_e32 v198, v199, v198
	v_mov_b32_e32 v202, v198
	v_mov_b32_e32 v201, v200
	s_nop 1
	v_permlane32_swap_b32 v202, v198
	s_nop 1
	s_nop 1
	v_permlane16_swap_b32 v201, v200
	s_nop 1
	v_add_f32_e32 v199, v201, v200
	v_mov_b32_e32 v203, v199
	s_nop 1
	v_permlane32_swap_b32 v203, v199
	s_nop 1
	s_and_saveexec_b64 s[4:5], s[6:7]
	v_lshlrev_b64 v[194:195], 8, v[192:193]
	v_lshl_add_u64 v[194:195], s[16:17], 0, v[194:195]
	v_lshl_add_u64 v[194:195], s[68:69], 3, v[194:195]
	v_pk_add_f32 v[200:201], v[202:203], v[198:199]
	global_store_dwordx2 v[194:195], v[200:201], off
	s_or_b64 exec, exec, s[4:5]

.LBB0_1808:
	s_cmp_gt_i32 s49, 10
	s_cselect_b64 s[4:5], -1, 0
	s_and_b64 s[0:1], s[10:11], s[4:5]
	s_andn2_b64 vcc, exec, s[0:1]
	s_cbranch_vccnz .LBB0_1958
	s_waitcnt vmcnt(0)
	s_waitcnt vmcnt(0) lgkmcnt(0)
	s_barrier
	s_getreg_b32 s0, hwreg(HW_REG_HW_ID, 0, 6)
	s_lshl_b32 s0, s0, 2
	s_and_b32 s0, s0, 0xfc
	s_add_i32 s0, s0, 0
	s_add_i32 s0, s0, 0x25c00
	v_mov_b32_e32 v0, s0
	ds_read_b32 v0, v0
	s_waitcnt lgkmcnt(0)
	v_readfirstlane_b32 s0, v0
	v_mbcnt_lo_u32_b32 v0, -1, 0
	v_mbcnt_hi_u32_b32 v0, -1, v0
	s_nop 1
	v_lshl_add_u32 v0, s0, 6, v0
	s_nop 0
	v_cmp_eq_u32_e32 vcc, 0, v0
	s_and_saveexec_b64 s[6:7], vcc
	s_cbranch_execz .LBB0_1837
	s_add_i32 s0, 0, 0x24800
	v_mov_b32_e32 v0, s0
	s_waitcnt vmcnt(0) expcnt(0) lgkmcnt(0)
	ds_read_b32 v1, v0
	s_add_i32 s0, 0, 0x24804
	v_mov_b32_e32 v0, s0
	ds_read_b32 v0, v0
	s_waitcnt lgkmcnt(1)
	v_cmp_ne_u32_e32 vcc, 0, v1
	s_cbranch_vccz .Lcensus_7

.LBB0_1973:
	s_cmp_gt_i32 s49, 11
	s_cselect_b64 s[6:7], -1, 0
	s_and_b64 s[0:1], s[10:11], s[6:7]
	s_andn2_b64 vcc, exec, s[0:1]
	s_cbranch_vccnz .LBB0_2123
	s_waitcnt vmcnt(0)
	s_waitcnt vmcnt(0) lgkmcnt(0)
	s_barrier
	s_getreg_b32 s0, hwreg(HW_REG_HW_ID, 0, 6)
	s_lshl_b32 s0, s0, 2
	s_and_b32 s0, s0, 0xfc
	s_add_i32 s0, s0, 0
	s_add_i32 s0, s0, 0x25c00
	v_mov_b32_e32 v0, s0
	ds_read_b32 v0, v0
	s_waitcnt lgkmcnt(0)
	v_readfirstlane_b32 s0, v0
	v_mbcnt_lo_u32_b32 v0, -1, 0
	v_mbcnt_hi_u32_b32 v0, -1, v0
	s_nop 1
	v_lshl_add_u32 v0, s0, 6, v0
	s_nop 0
	v_cmp_eq_u32_e32 vcc, 0, v0
	s_and_saveexec_b64 s[4:5], vcc
	s_cbranch_execz .LBB0_2002
	s_add_i32 s0, 0, 0x24800
	v_mov_b32_e32 v0, s0
	s_waitcnt vmcnt(0) expcnt(0) lgkmcnt(0)
	ds_read_b32 v1, v0
	s_add_i32 s0, 0, 0x24804
	v_mov_b32_e32 v0, s0
	ds_read_b32 v0, v0
	s_waitcnt lgkmcnt(1)
	v_cmp_ne_u32_e32 vcc, 0, v1
	s_cbranch_vccz .Lcensus_8

.LBB0_2108:
	v_readlane_b32 s3, v249, 34
	s_lshl_b32 s3, s3, 8
	s_waitcnt vmcnt(0)
	buffer_inv sc1
	s_waitcnt vmcnt(0)
	s_add_u32 s3, s94, s3
	s_addc_u32 s5, s95, 0
	s_add_u32 s4, s3, 0x2400
	s_addc_u32 s5, s5, 0
	s_mov_b64 s[12:13], -1
	s_mov_b64 s[10:11], exec
	v_mbcnt_lo_u32_b32 v0, s10, 0
	v_mbcnt_hi_u32_b32 v0, s11, v0
	v_cmp_eq_u32_e32 vcc, 0, v0
	s_and_b64 s[12:13], exec, vcc
	s_mov_b64 exec, s[12:13]
	s_cbranch_execz .LBB0_2122
	s_bcnt1_i32_b64 s3, s[10:11]
	v_mov_b32_e32 v0, 0
	v_mov_b32_e32 v1, s3
	global_atomic_add v0, v1, s[4:5]
	s_branch .LBB0_2122

.LBB0_2144:
	s_cmp_gt_i32 s49, 12
	s_cselect_b64 s[12:13], -1, 0
	s_and_b64 s[0:1], s[10:11], s[12:13]
	s_andn2_b64 vcc, exec, s[0:1]
	s_cbranch_vccnz .LBB0_2302
	s_waitcnt vmcnt(0)
	s_waitcnt vmcnt(0) lgkmcnt(0)
	s_barrier
	s_getreg_b32 s0, hwreg(HW_REG_HW_ID, 0, 6)
	s_lshl_b32 s0, s0, 2
	s_and_b32 s0, s0, 0xfc
	s_add_i32 s0, s0, 0
	s_add_i32 s0, s0, 0x25c00
	v_mov_b32_e32 v0, s0
	ds_read_b32 v0, v0
	s_waitcnt lgkmcnt(0)
	v_readfirstlane_b32 s0, v0
	v_mbcnt_lo_u32_b32 v0, -1, 0
	v_mbcnt_hi_u32_b32 v0, -1, v0
	s_nop 1
	v_lshl_add_u32 v0, s0, 6, v0
	s_nop 0
	v_cmp_eq_u32_e32 vcc, 0, v0
	s_and_saveexec_b64 s[6:7], vcc
	s_cbranch_execz .LBB0_2173
	s_add_i32 s0, 0, 0x24800
	v_mov_b32_e32 v0, s0
	s_waitcnt vmcnt(0) expcnt(0) lgkmcnt(0)
	ds_read_b32 v1, v0
	s_add_i32 s0, 0, 0x24804
	v_mov_b32_e32 v0, s0
	ds_read_b32 v0, v0
	s_waitcnt lgkmcnt(1)
	v_cmp_ne_u32_e32 vcc, 0, v1
	s_cbranch_vccz .Lcensus_9

.Lcensus_9:
	v_readlane_b32 s0, v249, 0
	v_readlane_b32 s1, v249, 1
	s_load_dwordx2 s[14:15], s[0:1], 0x4
	s_add_u32 s0, s94, 0x1000
	s_addc_u32 s1, s95, 0
	s_add_u32 s10, s94, 0x1100
	s_addc_u32 s11, s95, 0
	s_waitcnt lgkmcnt(0)
	s_mul_i32 s3, s14, s33
	s_add_u32 s14, s94, 0x1200
	s_mul_i32 s3, s3, s15
	s_addc_u32 s15, s95, 0
	s_add_u32 s16, s94, 0x1300
	s_addc_u32 s17, s95, 0
	s_mov_b32 s24, 1
	v_mov_b32_e32 v16, 0
	s_branch .LBB0_2149

.LBB0_2287:
	v_readlane_b32 s3, v249, 34
	s_lshl_b32 s3, s3, 8
	s_waitcnt vmcnt(0)
	buffer_inv sc1
	s_waitcnt vmcnt(0)
	s_add_u32 s3, s94, s3
	s_addc_u32 s7, s95, 0
	s_add_u32 s6, s3, 0x2400
	s_addc_u32 s7, s7, 0
	s_mov_b64 s[14:15], -1
	s_mov_b64 s[10:11], exec
	v_mbcnt_lo_u32_b32 v0, s10, 0
	v_mbcnt_hi_u32_b32 v0, s11, v0
	v_cmp_eq_u32_e32 vcc, 0, v0
	s_and_b64 s[14:15], exec, vcc
	s_mov_b64 exec, s[14:15]
	s_cbranch_execz .LBB0_2301
	s_bcnt1_i32_b64 s3, s[10:11]
	v_mov_b32_e32 v0, 0
	v_mov_b32_e32 v1, s3
	global_atomic_add v0, v1, s[6:7]
	s_branch .LBB0_2301

.LBB0_2335:
	s_cmp_gt_i32 s49, 13
	s_cselect_b64 s[4:5], -1, 0
	s_and_b64 s[0:1], s[14:15], s[4:5]
	s_andn2_b64 vcc, exec, s[0:1]
	s_cbranch_vccnz .LBB0_2397
	s_waitcnt vmcnt(0)
	s_waitcnt vmcnt(0) lgkmcnt(0)
	s_barrier
	s_getreg_b32 s0, hwreg(HW_REG_HW_ID, 0, 6)
	s_lshl_b32 s0, s0, 2
	s_and_b32 s0, s0, 0xfc
	s_add_i32 s0, s0, 0
	s_add_i32 s0, s0, 0x25c00
	v_mov_b32_e32 v0, s0
	ds_read_b32 v0, v0
	s_waitcnt lgkmcnt(0)
	v_readfirstlane_b32 s0, v0
	v_mbcnt_lo_u32_b32 v0, -1, 0
	v_mbcnt_hi_u32_b32 v0, -1, v0
	s_nop 1
	v_lshl_add_u32 v0, s0, 6, v0
	s_nop 0
	v_cmp_eq_u32_e32 vcc, 0, v0
	s_and_saveexec_b64 s[12:13], vcc
	s_cbranch_execz .LBB0_2366
	s_add_i32 s0, 0, 0x24800
	v_mov_b32_e32 v0, s0
	s_waitcnt vmcnt(0) expcnt(0) lgkmcnt(0)
	ds_read_b32 v1, v0
	s_add_i32 s0, 0, 0x24804
	v_mov_b32_e32 v0, s0
	ds_read_b32 v0, v0
	s_waitcnt lgkmcnt(1)
	v_cmp_ne_u32_e32 vcc, 0, v1
	s_cbranch_vccz .Lcensus_10

.LBB0_2762:
	v_readlane_b32 s4, v249, 51
	v_readlane_b32 s5, v249, 52
	s_mov_b64 s[44:45], s[4:5]
	s_cmp_lt_i32 s44, 15
	v_readlane_b32 s6, v249, 53
	v_readlane_b32 s7, v249, 54
	s_cselect_b64 s[0:1], -1, 0
	s_cmp_gt_i32 s45, 15
	s_cselect_b64 s[6:7], -1, 0
	s_and_b64 s[0:1], s[0:1], s[6:7]
	s_andn2_b64 vcc, exec, s[0:1]
	s_cbranch_vccnz .LBB0_2822
	s_waitcnt vmcnt(0)
	s_waitcnt vmcnt(0) lgkmcnt(0)
	s_barrier
	s_getreg_b32 s0, hwreg(HW_REG_HW_ID, 0, 6)
	s_lshl_b32 s0, s0, 2
	s_and_b32 s0, s0, 0xfc
	s_add_i32 s0, s0, 0
	s_add_i32 s0, s0, 0x25c00
	v_mov_b32_e32 v0, s0
	ds_read_b32 v0, v0
	s_waitcnt lgkmcnt(0)
	v_readfirstlane_b32 s0, v0
	v_mbcnt_lo_u32_b32 v0, -1, 0
	v_mbcnt_hi_u32_b32 v0, -1, v0
	s_nop 1
	v_lshl_add_u32 v0, s0, 6, v0
	s_nop 0
	v_cmp_eq_u32_e32 vcc, 0, v0
	s_and_saveexec_b64 s[4:5], vcc
	s_cbranch_execz .LBB0_2791
	s_add_i32 s0, 0, 0x24800
	v_mov_b32_e32 v0, s0
	s_waitcnt vmcnt(0) expcnt(0) lgkmcnt(0)
	ds_read_b32 v1, v0
	s_add_i32 s0, 0, 0x24804
	v_mov_b32_e32 v0, s0
	ds_read_b32 v0, v0
	s_waitcnt lgkmcnt(1)
	v_cmp_ne_u32_e32 vcc, 0, v1
	s_cbranch_vccz .Lcensus_11

.LBB0_2866:
	s_cmp_gt_i32 s45, 16
	s_cselect_b64 s[0:1], -1, 0
	s_and_b64 s[0:1], s[4:5], s[0:1]
	s_andn2_b64 vcc, exec, s[0:1]
	s_cbranch_vccnz .LBB0_2926
	s_waitcnt vmcnt(0)
	s_waitcnt vmcnt(0) lgkmcnt(0)
	s_barrier
	s_getreg_b32 s0, hwreg(HW_REG_HW_ID, 0, 6)
	s_lshl_b32 s0, s0, 2
	s_and_b32 s0, s0, 0xfc
	s_add_i32 s0, s0, 0
	s_add_i32 s0, s0, 0x25c00
	v_mov_b32_e32 v0, s0
	ds_read_b32 v0, v0
	s_waitcnt lgkmcnt(0)
	v_readfirstlane_b32 s0, v0
	v_mbcnt_lo_u32_b32 v0, -1, 0
	v_mbcnt_hi_u32_b32 v0, -1, v0
	s_nop 1
	v_lshl_add_u32 v0, s0, 6, v0
	s_nop 0
	v_cmp_eq_u32_e32 vcc, 0, v0
	s_and_saveexec_b64 s[2:3], vcc
	s_cbranch_execz .LBB0_2895
	s_add_i32 s0, 0, 0x24800
	v_mov_b32_e32 v0, s0
	s_waitcnt vmcnt(0) expcnt(0) lgkmcnt(0)
	ds_read_b32 v1, v0
	s_add_i32 s0, 0, 0x24804
	v_mov_b32_e32 v0, s0
	ds_read_b32 v0, v0
	s_waitcnt lgkmcnt(1)
	v_cmp_ne_u32_e32 vcc, 0, v1
	s_cbranch_vccz .Lcensus_12

.Lcensus_12:
	v_readlane_b32 s0, v249, 0
	v_readlane_b32 s1, v249, 1
	s_load_dwordx2 s[6:7], s[0:1], 0x4
	s_add_u32 s0, s94, 0x1000
	s_addc_u32 s1, s95, 0
	s_add_u32 s4, s94, 0x1100
	s_addc_u32 s5, s95, 0
	s_waitcnt lgkmcnt(0)
	s_mul_i32 s16, s6, s33
	s_add_u32 s6, s94, 0x1200
	s_mul_i32 s16, s16, s7
	s_addc_u32 s7, s95, 0
	s_add_u32 s8, s94, 0x1300
	s_addc_u32 s9, s95, 0
	s_mov_b32 s17, 1
	v_mov_b32_e32 v16, 0
	s_branch .LBB0_2871

.LBB0_2911:
	v_readlane_b32 s2, v249, 34
	s_lshl_b32 s2, s2, 8
	s_waitcnt vmcnt(0)
	buffer_inv sc1
	s_waitcnt vmcnt(0)
	s_add_u32 s2, s94, s2
	s_addc_u32 s3, s95, 0
	s_add_u32 s2, s2, 0x2400
	s_addc_u32 s3, s3, 0
	s_mov_b64 s[6:7], -1
	s_mov_b64 s[4:5], exec
	v_mbcnt_lo_u32_b32 v0, s4, 0
	v_mbcnt_hi_u32_b32 v0, s5, v0
	v_cmp_eq_u32_e32 vcc, 0, v0
	s_and_b64 s[6:7], exec, vcc
	s_mov_b64 exec, s[6:7]
	s_cbranch_execz .LBB0_2925
	s_bcnt1_i32_b64 s4, s[4:5]
	v_mov_b32_e32 v0, 0
	v_mov_b32_e32 v1, s4
	global_atomic_add v0, v1, s[2:3]
	s_branch .LBB0_2925
